# res1: rot1 + Wo / cross-attention-output residual epilogues request both 128-row halves' residual rows up front (one round trip instead of two)
# speedup vs baseline: 1.0083x; 1.0083x over previous
; __device__ __forceinline__ unsigned cvt_pk_bf16(float lo, float hi) { unsigned r; asm volatile("v_cvt_pk_bf16_f32 %0, %1, %2" : "=v"(r) : "v"(lo), "v"(hi)); return r; }
; __device__ __forceinline__ float bf_lo(unsigned w) { return __uint_as_float(w << 16); }
; __device__ __forceinline__ float bf_hi(unsigned w) { return __uint_as_float(w & 0xffff0000u); }
; template <int M> __device__ __forceinline__ float swz_xor(float v) { return __int_as_float(__builtin_amdgcn_ds_swizzle(__float_as_int(v), (M << 10) | 0x1f)); }
; __device__ __forceinline__ float half_sum(float v) { auto rr = __builtin_amdgcn_permlane32_swap(__float_as_uint(v), __float_as_uint(v), false, false); return __uint_as_float(rr[0]) + __uint_as_float(rr[1]); }
; __device__ __forceinline__ void st16_wt(void* p, u32x4 w) { asm volatile("global_store_dwordx4 %0, %1, off sc1\n\ts_nop 1" :: "v"(p), "v"(w) : "memory"); }
;     __device__ __forceinline__ bool operator()(f32x4 (&acc)[2][2][4][2], const pg8::Unit& u, int wr, int wc, int fr, int fq) const {
;         const int row0 = u.pm * 256 + wr * 64 + fr, colb = u.pn * 256 + wc * 32 + 8 * fq;
; #pragma unroll
;         for (int ai = 0; ai < 2; ++ai) {
;             u32x4 xin[4][2];
; #pragma unroll
;             for (int m = 0; m < 4; ++m)
; #pragma unroll
;                 for (int bj = 0; bj < 2; ++bj) xin[m][bj] = *(const u32x4*)(xbase + (size_t)(row0 + ai * 128 + m * 16) * DM + colb + bj * 128);
; #pragma unroll
;             for (int m = 0; m < 4; ++m) { const int row = row0 + ai * 128 + m * 16; float ss = 0.f;
; #pragma unroll
;                 for (int bj = 0; bj < 2; ++bj) { const size_t off = (size_t)row * DM + colb + bj * 128; const u32x4 xw = xin[m][bj];
;                     f32x4 a = {bf_lo(xw.x), bf_hi(xw.x), bf_lo(xw.y), bf_hi(xw.y)}, b = {bf_lo(xw.z), bf_hi(xw.z), bf_lo(xw.w), bf_hi(xw.w)};
;                     a += acc[ai][bj][m][0]; b += acc[ai][bj][m][1];
;                     ss += ((a[0] * a[0] + a[1] * a[1]) + (a[2] * a[2] + a[3] * a[3])) + ((b[0] * b[0] + b[1] * b[1]) + (b[2] * b[2] + b[3] * b[3]));
;                     { u32x4 w; w.x = cvt_pk_bf16(a[0], a[1]); w.y = cvt_pk_bf16(a[2], a[3]); w.z = cvt_pk_bf16(b[0], b[1]); w.w = cvt_pk_bf16(b[2], b[3]); st16_wt(xb + off, w); } }
;                 ss += swz_xor<16>(ss); ss = half_sum(ss);
;                 if (fq == 0) xch[(ai * 128 + wr * 64 + m * 16 + fr) * 4 + wc] = ss; } }
.LBB0_1031:
	s_lshl_b32 s7, s44, 8
	v_lshl_or_b32 v164, s45, 8, v183
	v_add_u32_e32 v168, s7, v180
	v_ashrrev_i32_e32 v165, 31, v164
	v_readlane_b32 s2, v252, 8
	v_lshlrev_b64 v[176:177], 1, v[164:165]
	v_readlane_b32 s3, v252, 9
	v_ashrrev_i32_e32 v169, 31, v168
	v_lshlrev_b64 v[178:179], 11, v[168:169]
	v_lshl_add_u64 v[166:167], s[2:3], 0, v[176:177]
	v_lshl_add_u64 v[128:129], v[166:167], 0, v[178:179]
	global_load_dwordx4 v[196:199], v[128:129], off
	global_load_dwordx4 v[152:155], v[128:129], off offset:256
	v_or_b32_e32 v128, 16, v168
	v_ashrrev_i32_e32 v129, 31, v128
	v_lshlrev_b64 v[174:175], 11, v[128:129]
	v_lshl_add_u64 v[128:129], v[166:167], 0, v[174:175]
	global_load_dwordx4 v[148:151], v[128:129], off
	global_load_dwordx4 v[144:147], v[128:129], off offset:256
	v_or_b32_e32 v128, 32, v168
	v_ashrrev_i32_e32 v129, 31, v128
	v_lshlrev_b64 v[172:173], 11, v[128:129]
	v_lshl_add_u64 v[128:129], v[166:167], 0, v[172:173]
	global_load_dwordx4 v[140:143], v[128:129], off
	global_load_dwordx4 v[136:139], v[128:129], off offset:256
	v_or_b32_e32 v128, 48, v168
	v_ashrrev_i32_e32 v129, 31, v128
	v_lshlrev_b64 v[170:171], 11, v[128:129]
	v_lshl_add_u64 v[128:129], v[166:167], 0, v[170:171]
	global_load_dwordx4 v[132:135], v[128:129], off
	s_nop 0
	global_load_dwordx4 v[128:131], v[128:129], off offset:256
	v_lshlrev_b32_e32 v232, 11, v168
	v_mov_b32_e32 v233, 0
	v_add_u32_e32 v232, 0x40000, v232
	v_lshl_add_u64 v[234:235], v[166:167], 0, v[232:233]
	global_load_dwordx4 v[200:203], v[234:235], off
	global_load_dwordx4 v[204:207], v[234:235], off offset:256
	v_add_u32_e32 v232, 0x8000, v232
	v_lshl_add_u64 v[234:235], v[166:167], 0, v[232:233]
	global_load_dwordx4 v[208:211], v[234:235], off
	global_load_dwordx4 v[216:219], v[234:235], off offset:256
	v_add_u32_e32 v232, 0x8000, v232
	v_lshl_add_u64 v[234:235], v[166:167], 0, v[232:233]
	global_load_dwordx4 v[220:223], v[234:235], off
	global_load_dwordx4 v[224:227], v[234:235], off offset:256
	v_add_u32_e32 v232, 0x8000, v232
	v_lshl_add_u64 v[234:235], v[166:167], 0, v[232:233]
	global_load_dwordx4 v[240:243], v[234:235], off
	global_load_dwordx4 v[244:247], v[234:235], off offset:256
	s_waitcnt vmcnt(0)
	v_lshlrev_b32_e32 v188, 16, v196
	v_and_b32_e32 v189, 0xffff0000, v196
	v_lshlrev_b32_e32 v190, 16, v197
	v_and_b32_e32 v191, 0xffff0000, v197
	v_lshlrev_b32_e32 v192, 16, v198
	v_and_b32_e32 v193, 0xffff0000, v198
	v_lshlrev_b32_e32 v196, 16, v199
	v_and_b32_e32 v197, 0xffff0000, v199
	v_pk_add_f32 v[126:127], v[126:127], v[190:191]
	v_pk_add_f32 v[124:125], v[124:125], v[188:189]
	v_pk_add_f32 v[188:189], v[122:123], v[196:197]
	v_pk_add_f32 v[122:123], v[120:121], v[192:193]
	v_mul_f32_e32 v120, v125, v125
	v_mul_f32_e32 v121, v127, v127
	v_fmac_f32_e32 v120, v124, v124
	v_fmac_f32_e32 v121, v126, v126
	v_add_f32_e32 v120, v120, v121
	v_mul_f32_e32 v121, v123, v123
	v_mul_f32_e32 v187, v189, v189
	v_fmac_f32_e32 v121, v122, v122
	v_fmac_f32_e32 v187, v188, v188
	v_add_f32_e32 v121, v121, v187
	v_add_f32_e32 v187, v120, v121
	v_cvt_pk_bf16_f32 v120, v124, v125
	v_cvt_pk_bf16_f32 v121, v126, v127
	v_cvt_pk_bf16_f32 v122, v122, v123
	v_cvt_pk_bf16_f32 v123, v188, v189
	v_lshl_add_u64 v[124:125], s[2:3], 0, v[178:179]
	v_lshl_add_u64 v[124:125], v[124:125], 0, v[176:177]
	global_store_dwordx4 v[124:125], v[120:123], off sc1
	s_nop 1
	v_lshlrev_b32_e32 v120, 16, v152
	v_and_b32_e32 v121, 0xffff0000, v152
	v_lshlrev_b32_e32 v122, 16, v153
	v_and_b32_e32 v123, 0xffff0000, v153
	v_lshlrev_b32_e32 v126, 16, v154
	v_and_b32_e32 v127, 0xffff0000, v154
	v_lshlrev_b32_e32 v152, 16, v155
	v_and_b32_e32 v153, 0xffff0000, v155
	v_pk_add_f32 v[118:119], v[118:119], v[122:123]
	v_pk_add_f32 v[116:117], v[116:117], v[120:121]
	v_pk_add_f32 v[120:121], v[114:115], v[152:153]
	v_pk_add_f32 v[114:115], v[112:113], v[126:127]
	v_mul_f32_e32 v112, v117, v117
	v_mul_f32_e32 v113, v119, v119
	v_fmac_f32_e32 v112, v116, v116
	v_fmac_f32_e32 v113, v118, v118
	v_add_f32_e32 v112, v112, v113
	v_mul_f32_e32 v113, v115, v115
	v_mul_f32_e32 v122, v121, v121
	v_fmac_f32_e32 v113, v114, v114
	v_fmac_f32_e32 v122, v120, v120
	v_add_f32_e32 v113, v113, v122
	v_add_f32_e32 v112, v112, v113
	v_add_f32_e32 v122, v187, v112
	v_cvt_pk_bf16_f32 v112, v116, v117
	s_mov_b64 s[2:3], 0x100
	v_cvt_pk_bf16_f32 v113, v118, v119
	v_cvt_pk_bf16_f32 v114, v114, v115
	v_cvt_pk_bf16_f32 v115, v120, v121
	v_lshl_add_u64 v[116:117], v[124:125], 0, s[2:3]
	global_store_dwordx4 v[116:117], v[112:115], off sc1
	s_nop 1
	ds_swizzle_b32 v112, v122 offset:swizzle(SWAP,16)
	s_waitcnt lgkmcnt(0)
; __device__ __forceinline__ unsigned cvt_pk_bf16(float lo, float hi) { unsigned r; asm volatile("v_cvt_pk_bf16_f32 %0, %1, %2" : "=v"(r) : "v"(lo), "v"(hi)); return r; }
; __device__ __forceinline__ float bf_lo(unsigned w) { return __uint_as_float(w << 16); }
; __device__ __forceinline__ float bf_hi(unsigned w) { return __uint_as_float(w & 0xffff0000u); }
; template <int M> __device__ __forceinline__ float swz_xor(float v) { return __int_as_float(__builtin_amdgcn_ds_swizzle(__float_as_int(v), (M << 10) | 0x1f)); }
; __device__ __forceinline__ float half_sum(float v) { auto rr = __builtin_amdgcn_permlane32_swap(__float_as_uint(v), __float_as_uint(v), false, false); return __uint_as_float(rr[0]) + __uint_as_float(rr[1]); }
; __device__ __forceinline__ void st16_wt(void* p, u32x4 w) { asm volatile("global_store_dwordx4 %0, %1, off sc1\n\ts_nop 1" :: "v"(p), "v"(w) : "memory"); }
;     __device__ __forceinline__ bool operator()(f32x4 (&acc)[2][2][4][2], const pg8::Unit& u, int wr, int wc, int fr, int fq) const {
;     ...
;             for (int m = 0; m < 4; ++m) { const int row = row0 + ai * 128 + m * 16; float ss = 0.f;
; #pragma unroll
;                 for (int bj = 0; bj < 2; ++bj) { const size_t off = (size_t)row * DM + colb + bj * 128; const u32x4 xw = xin[m][bj];
;                     f32x4 a = {bf_lo(xw.x), bf_hi(xw.x), bf_lo(xw.y), bf_hi(xw.y)}, b = {bf_lo(xw.z), bf_hi(xw.z), bf_lo(xw.w), bf_hi(xw.w)};
;                     a += acc[ai][bj][m][0]; b += acc[ai][bj][m][1];
;                     ss += ((a[0] * a[0] + a[1] * a[1]) + (a[2] * a[2] + a[3] * a[3])) + ((b[0] * b[0] + b[1] * b[1]) + (b[2] * b[2] + b[3] * b[3]));
;                     { u32x4 w; w.x = cvt_pk_bf16(a[0], a[1]); w.y = cvt_pk_bf16(a[2], a[3]); w.z = cvt_pk_bf16(b[0], b[1]); w.w = cvt_pk_bf16(b[2], b[3]); st16_wt(xb + off, w); } }
;                 ss += swz_xor<16>(ss); ss = half_sum(ss);
;                 if (fq == 0) xch[(ai * 128 + wr * 64 + m * 16 + fr) * 4 + wc] = ss; } }
	v_add_f32_e32 v112, v122, v112
	v_mov_b32_e32 v113, v112
	s_nop 1
	v_permlane32_swap_b32_e32 v112, v113
	s_and_saveexec_b64 s[4:5], s[10:11]
	v_add_f32_e32 v112, v112, v113
	ds_write_b32 v186, v112
	s_or_b64 exec, exec, s[4:5]
	v_lshlrev_b32_e32 v112, 16, v148
	v_and_b32_e32 v113, 0xffff0000, v148
	v_lshlrev_b32_e32 v114, 16, v149
	v_and_b32_e32 v115, 0xffff0000, v149
	v_lshlrev_b32_e32 v116, 16, v150
	v_and_b32_e32 v117, 0xffff0000, v150
	v_lshlrev_b32_e32 v118, 16, v151
	v_and_b32_e32 v119, 0xffff0000, v151
	v_pk_add_f32 v[110:111], v[110:111], v[114:115]
	v_pk_add_f32 v[108:109], v[108:109], v[112:113]
	v_pk_add_f32 v[112:113], v[106:107], v[118:119]
	v_pk_add_f32 v[106:107], v[104:105], v[116:117]
	v_mul_f32_e32 v104, v109, v109
	v_mul_f32_e32 v105, v111, v111
	v_fmac_f32_e32 v104, v108, v108
	v_fmac_f32_e32 v105, v110, v110
	v_add_f32_e32 v104, v104, v105
	v_mul_f32_e32 v105, v107, v107
	v_mul_f32_e32 v114, v113, v113
	v_fmac_f32_e32 v105, v106, v106
	v_fmac_f32_e32 v114, v112, v112
	v_readlane_b32 s2, v252, 8
	v_add_f32_e32 v105, v105, v114
	v_readlane_b32 s3, v252, 9
	v_add_f32_e32 v114, v104, v105
	v_cvt_pk_bf16_f32 v104, v108, v109
	v_cvt_pk_bf16_f32 v105, v110, v111
	v_cvt_pk_bf16_f32 v106, v106, v107
	v_cvt_pk_bf16_f32 v107, v112, v113
	s_nop 0
	v_lshl_add_u64 v[108:109], s[2:3], 0, v[174:175]
	v_lshl_add_u64 v[108:109], v[164:165], 1, v[108:109]
	global_store_dwordx4 v[108:109], v[104:107], off sc1
	s_nop 1
	v_lshlrev_b32_e32 v104, 16, v144
	v_and_b32_e32 v105, 0xffff0000, v144
	v_lshlrev_b32_e32 v106, 16, v145
	v_and_b32_e32 v107, 0xffff0000, v145
	v_lshlrev_b32_e32 v110, 16, v146
	v_and_b32_e32 v111, 0xffff0000, v146
	v_lshlrev_b32_e32 v112, 16, v147
	v_and_b32_e32 v113, 0xffff0000, v147
	v_pk_add_f32 v[102:103], v[102:103], v[106:107]
	v_pk_add_f32 v[100:101], v[100:101], v[104:105]
	v_pk_add_f32 v[104:105], v[98:99], v[112:113]
	v_pk_add_f32 v[98:99], v[96:97], v[110:111]
	v_mul_f32_e32 v96, v101, v101
	v_mul_f32_e32 v97, v103, v103
	v_fmac_f32_e32 v96, v100, v100
	v_fmac_f32_e32 v97, v102, v102
	v_add_f32_e32 v96, v96, v97
	v_mul_f32_e32 v97, v99, v99
	v_mul_f32_e32 v106, v105, v105
	v_fmac_f32_e32 v97, v98, v98
	v_fmac_f32_e32 v106, v104, v104
	v_add_f32_e32 v97, v97, v106
	v_add_f32_e32 v96, v96, v97
	v_add_f32_e32 v106, v114, v96
	v_cvt_pk_bf16_f32 v96, v100, v101
	v_cvt_pk_bf16_f32 v97, v102, v103
	v_mov_b32_e32 v102, v106
	s_mov_b64 s[2:3], 0x100
	v_cvt_pk_bf16_f32 v98, v98, v99
	v_cvt_pk_bf16_f32 v99, v104, v105
	v_lshl_add_u64 v[100:101], v[108:109], 0, s[2:3]
	global_store_dwordx4 v[100:101], v[96:99], off sc1
	s_nop 1
	s_waitcnt lgkmcnt(0)
	s_nop 1
	v_permlane16_swap_b32_e32 v102, v106
	v_add_f32_e32 v96, v106, v102
	v_mov_b32_e32 v97, v96
	s_nop 1
	v_permlane32_swap_b32_e32 v96, v97
	s_and_saveexec_b64 s[4:5], s[10:11]
	v_add_f32_e32 v96, v96, v97
	ds_write_b32 v186, v96 offset:256
	s_or_b64 exec, exec, s[4:5]
	v_lshlrev_b32_e32 v96, 16, v140
	v_and_b32_e32 v97, 0xffff0000, v140
	v_lshlrev_b32_e32 v98, 16, v141
	v_and_b32_e32 v99, 0xffff0000, v141
	v_lshlrev_b32_e32 v100, 16, v142
	v_and_b32_e32 v101, 0xffff0000, v142
	v_lshlrev_b32_e32 v102, 16, v143
	v_and_b32_e32 v103, 0xffff0000, v143
	v_pk_add_f32 v[94:95], v[94:95], v[98:99]
	v_pk_add_f32 v[92:93], v[92:93], v[96:97]
	v_pk_add_f32 v[96:97], v[90:91], v[102:103]
	v_pk_add_f32 v[90:91], v[88:89], v[100:101]
	v_mul_f32_e32 v88, v93, v93
	v_mul_f32_e32 v89, v95, v95
	v_fmac_f32_e32 v88, v92, v92
	v_fmac_f32_e32 v89, v94, v94
	v_add_f32_e32 v88, v88, v89
	v_mul_f32_e32 v89, v91, v91
	v_mul_f32_e32 v98, v97, v97
	v_fmac_f32_e32 v89, v90, v90
	v_fmac_f32_e32 v98, v96, v96
	v_readlane_b32 s2, v252, 8
	v_add_f32_e32 v89, v89, v98
	v_readlane_b32 s3, v252, 9
	v_add_f32_e32 v98, v88, v89
	v_cvt_pk_bf16_f32 v88, v92, v93
	v_cvt_pk_bf16_f32 v89, v94, v95
	v_cvt_pk_bf16_f32 v90, v90, v91
	v_cvt_pk_bf16_f32 v91, v96, v97
	s_nop 0
	v_lshl_add_u64 v[92:93], s[2:3], 0, v[172:173]
	v_lshl_add_u64 v[92:93], v[164:165], 1, v[92:93]
	global_store_dwordx4 v[92:93], v[88:91], off sc1
	s_nop 1
	v_lshlrev_b32_e32 v88, 16, v136
	v_and_b32_e32 v89, 0xffff0000, v136
	v_lshlrev_b32_e32 v90, 16, v137
	v_and_b32_e32 v91, 0xffff0000, v137
	v_lshlrev_b32_e32 v94, 16, v138
	v_and_b32_e32 v95, 0xffff0000, v138
	v_lshlrev_b32_e32 v96, 16, v139
	v_and_b32_e32 v97, 0xffff0000, v139
	v_pk_add_f32 v[86:87], v[86:87], v[90:91]
	v_pk_add_f32 v[84:85], v[84:85], v[88:89]
	v_pk_add_f32 v[88:89], v[82:83], v[96:97]
	v_pk_add_f32 v[82:83], v[80:81], v[94:95]
	v_mul_f32_e32 v80, v85, v85
	v_mul_f32_e32 v81, v87, v87
	v_fmac_f32_e32 v80, v84, v84
	v_fmac_f32_e32 v81, v86, v86
	v_add_f32_e32 v80, v80, v81
	v_mul_f32_e32 v81, v83, v83
	v_mul_f32_e32 v90, v89, v89
	v_fmac_f32_e32 v81, v82, v82
	v_fmac_f32_e32 v90, v88, v88
	v_add_f32_e32 v81, v81, v90
	v_add_f32_e32 v80, v80, v81
	v_add_f32_e32 v90, v98, v80
	v_cvt_pk_bf16_f32 v80, v84, v85
	v_cvt_pk_bf16_f32 v81, v86, v87
	v_mov_b32_e32 v86, v90
	s_mov_b64 s[2:3], 0x100
	v_cvt_pk_bf16_f32 v82, v82, v83
	v_cvt_pk_bf16_f32 v83, v88, v89
	v_lshl_add_u64 v[84:85], v[92:93], 0, s[2:3]
	global_store_dwordx4 v[84:85], v[80:83], off sc1
	s_nop 1
	s_waitcnt lgkmcnt(0)
; __device__ __forceinline__ unsigned cvt_pk_bf16(float lo, float hi) { unsigned r; asm volatile("v_cvt_pk_bf16_f32 %0, %1, %2" : "=v"(r) : "v"(lo), "v"(hi)); return r; }
; __device__ __forceinline__ float bf_lo(unsigned w) { return __uint_as_float(w << 16); }
; __device__ __forceinline__ float bf_hi(unsigned w) { return __uint_as_float(w & 0xffff0000u); }
; template <int M> __device__ __forceinline__ float swz_xor(float v) { return __int_as_float(__builtin_amdgcn_ds_swizzle(__float_as_int(v), (M << 10) | 0x1f)); }
; __device__ __forceinline__ float half_sum(float v) { auto rr = __builtin_amdgcn_permlane32_swap(__float_as_uint(v), __float_as_uint(v), false, false); return __uint_as_float(rr[0]) + __uint_as_float(rr[1]); }
; __device__ __forceinline__ void st16_wt(void* p, u32x4 w) { asm volatile("global_store_dwordx4 %0, %1, off sc1\n\ts_nop 1" :: "v"(p), "v"(w) : "memory"); }
;     __device__ __forceinline__ bool operator()(f32x4 (&acc)[2][2][4][2], const pg8::Unit& u, int wr, int wc, int fr, int fq) const {
;     ...
;         for (int ai = 0; ai < 2; ++ai) {
;             u32x4 xin[4][2];
; #pragma unroll
;             for (int m = 0; m < 4; ++m)
; #pragma unroll
;                 for (int bj = 0; bj < 2; ++bj) xin[m][bj] = *(const u32x4*)(xbase + (size_t)(row0 + ai * 128 + m * 16) * DM + colb + bj * 128);
; #pragma unroll
;             for (int m = 0; m < 4; ++m) { const int row = row0 + ai * 128 + m * 16; float ss = 0.f;
; #pragma unroll
;                 for (int bj = 0; bj < 2; ++bj) { const size_t off = (size_t)row * DM + colb + bj * 128; const u32x4 xw = xin[m][bj];
;                     f32x4 a = {bf_lo(xw.x), bf_hi(xw.x), bf_lo(xw.y), bf_hi(xw.y)}, b = {bf_lo(xw.z), bf_hi(xw.z), bf_lo(xw.w), bf_hi(xw.w)};
;                     a += acc[ai][bj][m][0]; b += acc[ai][bj][m][1];
;                     ss += ((a[0] * a[0] + a[1] * a[1]) + (a[2] * a[2] + a[3] * a[3])) + ((b[0] * b[0] + b[1] * b[1]) + (b[2] * b[2] + b[3] * b[3]));
;                     { u32x4 w; w.x = cvt_pk_bf16(a[0], a[1]); w.y = cvt_pk_bf16(a[2], a[3]); w.z = cvt_pk_bf16(b[0], b[1]); w.w = cvt_pk_bf16(b[2], b[3]); st16_wt(xb + off, w); } }
;                 ss += swz_xor<16>(ss); ss = half_sum(ss);
;                 if (fq == 0) xch[(ai * 128 + wr * 64 + m * 16 + fr) * 4 + wc] = ss; } }
	s_nop 1
	v_permlane16_swap_b32_e32 v86, v90
	v_add_f32_e32 v80, v90, v86
	v_mov_b32_e32 v81, v80
	s_nop 1
	v_permlane32_swap_b32_e32 v80, v81
	s_and_saveexec_b64 s[4:5], s[10:11]
	v_add_f32_e32 v80, v80, v81
	ds_write_b32 v186, v80 offset:512
	s_or_b64 exec, exec, s[4:5]
	v_lshlrev_b32_e32 v80, 16, v132
	v_and_b32_e32 v81, 0xffff0000, v132
	v_lshlrev_b32_e32 v82, 16, v133
	v_and_b32_e32 v83, 0xffff0000, v133
	v_lshlrev_b32_e32 v84, 16, v134
	v_and_b32_e32 v85, 0xffff0000, v134
	v_lshlrev_b32_e32 v86, 16, v135
	v_and_b32_e32 v87, 0xffff0000, v135
	v_pk_add_f32 v[78:79], v[78:79], v[82:83]
	v_pk_add_f32 v[76:77], v[76:77], v[80:81]
	v_pk_add_f32 v[80:81], v[74:75], v[86:87]
	v_pk_add_f32 v[74:75], v[72:73], v[84:85]
	v_mul_f32_e32 v72, v77, v77
	v_mul_f32_e32 v73, v79, v79
	v_fmac_f32_e32 v72, v76, v76
	v_fmac_f32_e32 v73, v78, v78
	v_add_f32_e32 v72, v72, v73
	v_mul_f32_e32 v73, v75, v75
	v_mul_f32_e32 v82, v81, v81
	v_fmac_f32_e32 v73, v74, v74
	v_fmac_f32_e32 v82, v80, v80
	v_readlane_b32 s2, v252, 8
	v_add_f32_e32 v73, v73, v82
	v_readlane_b32 s3, v252, 9
	v_add_f32_e32 v82, v72, v73
	v_cvt_pk_bf16_f32 v72, v76, v77
	v_cvt_pk_bf16_f32 v73, v78, v79
	v_cvt_pk_bf16_f32 v74, v74, v75
	v_cvt_pk_bf16_f32 v75, v80, v81
	s_nop 0
	v_lshl_add_u64 v[76:77], s[2:3], 0, v[170:171]
	v_lshl_add_u64 v[76:77], v[164:165], 1, v[76:77]
	global_store_dwordx4 v[76:77], v[72:75], off sc1
	s_nop 1
	v_lshlrev_b32_e32 v72, 16, v128
	v_and_b32_e32 v73, 0xffff0000, v128
	v_lshlrev_b32_e32 v74, 16, v129
	v_and_b32_e32 v75, 0xffff0000, v129
	v_lshlrev_b32_e32 v78, 16, v130
	v_and_b32_e32 v79, 0xffff0000, v130
	v_lshlrev_b32_e32 v80, 16, v131
	v_and_b32_e32 v81, 0xffff0000, v131
	v_pk_add_f32 v[70:71], v[70:71], v[74:75]
	v_pk_add_f32 v[68:69], v[68:69], v[72:73]
	v_pk_add_f32 v[72:73], v[66:67], v[80:81]
	v_pk_add_f32 v[66:67], v[64:65], v[78:79]
	v_mul_f32_e32 v64, v69, v69
	v_mul_f32_e32 v65, v71, v71
	v_fmac_f32_e32 v64, v68, v68
	v_fmac_f32_e32 v65, v70, v70
	v_add_f32_e32 v64, v64, v65
	v_mul_f32_e32 v65, v67, v67
	v_mul_f32_e32 v74, v73, v73
	v_fmac_f32_e32 v65, v66, v66
	v_fmac_f32_e32 v74, v72, v72
	v_add_f32_e32 v65, v65, v74
	v_add_f32_e32 v64, v64, v65
	v_add_f32_e32 v74, v82, v64
	v_cvt_pk_bf16_f32 v64, v68, v69
	v_cvt_pk_bf16_f32 v65, v70, v71
	v_mov_b32_e32 v70, v74
	s_mov_b64 s[2:3], 0x100
	v_cvt_pk_bf16_f32 v66, v66, v67
	v_cvt_pk_bf16_f32 v67, v72, v73
	v_lshl_add_u64 v[68:69], v[76:77], 0, s[2:3]
	global_store_dwordx4 v[68:69], v[64:67], off sc1
	s_nop 1
	s_waitcnt lgkmcnt(0)
	s_nop 1
	v_permlane16_swap_b32_e32 v70, v74
	v_add_f32_e32 v64, v74, v70
	v_mov_b32_e32 v65, v64
	s_nop 1
	v_permlane32_swap_b32_e32 v64, v65
	s_and_saveexec_b64 s[4:5], s[10:11]
	v_add_f32_e32 v64, v64, v65
	ds_write_b32 v186, v64 offset:768
	s_or_b64 exec, exec, s[4:5]
	v_lshlrev_b64 v[64:65], 11, v[168:169]
	s_mov_b64 s[2:3], 0x40000
	v_lshl_add_u64 v[102:103], v[64:65], 0, s[2:3]
	v_lshl_add_u64 v[66:67], v[166:167], 0, v[102:103]
	s_mov_b64 s[2:3], 0x48000
	v_lshl_add_u64 v[92:93], v[64:65], 0, s[2:3]
	s_mov_b64 s[2:3], 0x50000
	v_lshl_add_u64 v[90:91], v[64:65], 0, s[2:3]
	s_mov_b64 s[2:3], 0x58000
	v_lshl_add_u64 v[66:67], v[166:167], 0, v[92:93]
	v_lshl_add_u64 v[88:89], v[64:65], 0, s[2:3]
	v_lshl_add_u64 v[66:67], v[166:167], 0, v[90:91]
	v_lshl_add_u64 v[64:65], v[166:167], 0, v[88:89]
	v_readlane_b32 s2, v252, 8
	v_readlane_b32 s3, v252, 9
	v_lshlrev_b32_e32 v104, 16, v200
	v_and_b32_e32 v105, 0xffff0000, v200
	v_lshlrev_b32_e32 v94, 16, v201
	v_and_b32_e32 v95, 0xffff0000, v201
	v_lshlrev_b32_e32 v106, 16, v202
	v_and_b32_e32 v107, 0xffff0000, v202
	v_lshlrev_b32_e32 v96, 16, v203
	v_and_b32_e32 v97, 0xffff0000, v203
	v_pk_add_f32 v[62:63], v[62:63], v[94:95]
	v_pk_add_f32 v[60:61], v[60:61], v[104:105]
	v_pk_add_f32 v[94:95], v[58:59], v[96:97]
	v_pk_add_f32 v[58:59], v[56:57], v[106:107]
	v_mul_f32_e32 v56, v61, v61
	v_mul_f32_e32 v57, v63, v63
	v_fmac_f32_e32 v56, v60, v60
	v_fmac_f32_e32 v57, v62, v62
	v_add_f32_e32 v56, v56, v57
	v_mul_f32_e32 v57, v59, v59
	v_mul_f32_e32 v96, v95, v95
	v_fmac_f32_e32 v57, v58, v58
	v_fmac_f32_e32 v96, v94, v94
	v_add_f32_e32 v57, v57, v96
	v_add_f32_e32 v96, v56, v57
	v_cvt_pk_bf16_f32 v56, v60, v61
	v_cvt_pk_bf16_f32 v57, v62, v63
	v_cvt_pk_bf16_f32 v58, v58, v59
	v_cvt_pk_bf16_f32 v59, v94, v95
	v_lshl_add_u64 v[60:61], s[2:3], 0, v[102:103]
	v_lshl_add_u64 v[60:61], v[164:165], 1, v[60:61]
	global_store_dwordx4 v[60:61], v[56:59], off sc1
	s_nop 1
	v_lshlrev_b32_e32 v56, 16, v204
	v_and_b32_e32 v57, 0xffff0000, v204
	v_lshlrev_b32_e32 v58, 16, v205
	v_and_b32_e32 v59, 0xffff0000, v205
	v_lshlrev_b32_e32 v62, 16, v206
	v_and_b32_e32 v63, 0xffff0000, v206
	v_lshlrev_b32_e32 v94, 16, v207
	v_and_b32_e32 v95, 0xffff0000, v207
	v_pk_add_f32 v[54:55], v[54:55], v[58:59]
	v_pk_add_f32 v[52:53], v[52:53], v[56:57]
	v_pk_add_f32 v[56:57], v[50:51], v[94:95]
	v_pk_add_f32 v[50:51], v[48:49], v[62:63]
	v_mul_f32_e32 v48, v53, v53
	v_mul_f32_e32 v49, v55, v55
	v_fmac_f32_e32 v48, v52, v52
	v_fmac_f32_e32 v49, v54, v54
	v_add_f32_e32 v48, v48, v49
	v_mul_f32_e32 v49, v51, v51
	v_mul_f32_e32 v58, v57, v57
	v_fmac_f32_e32 v49, v50, v50
	v_fmac_f32_e32 v58, v56, v56
	v_add_f32_e32 v49, v49, v58
	v_add_f32_e32 v48, v48, v49
	v_add_f32_e32 v58, v96, v48
	v_cvt_pk_bf16_f32 v48, v52, v53
	s_mov_b64 s[2:3], 0x100
	v_cvt_pk_bf16_f32 v49, v54, v55
	v_cvt_pk_bf16_f32 v50, v50, v51
	v_cvt_pk_bf16_f32 v51, v56, v57
	v_lshl_add_u64 v[52:53], v[60:61], 0, s[2:3]
	global_store_dwordx4 v[52:53], v[48:51], off sc1
	s_nop 1
	ds_swizzle_b32 v48, v58 offset:swizzle(SWAP,16)
	s_waitcnt lgkmcnt(0)
; __device__ __forceinline__ unsigned cvt_pk_bf16(float lo, float hi) { unsigned r; asm volatile("v_cvt_pk_bf16_f32 %0, %1, %2" : "=v"(r) : "v"(lo), "v"(hi)); return r; }
; __device__ __forceinline__ float bf_lo(unsigned w) { return __uint_as_float(w << 16); }
; __device__ __forceinline__ float bf_hi(unsigned w) { return __uint_as_float(w & 0xffff0000u); }
; template <int M> __device__ __forceinline__ float swz_xor(float v) { return __int_as_float(__builtin_amdgcn_ds_swizzle(__float_as_int(v), (M << 10) | 0x1f)); }
; __device__ __forceinline__ float half_sum(float v) { auto rr = __builtin_amdgcn_permlane32_swap(__float_as_uint(v), __float_as_uint(v), false, false); return __uint_as_float(rr[0]) + __uint_as_float(rr[1]); }
; __device__ __forceinline__ void st16_wt(void* p, u32x4 w) { asm volatile("global_store_dwordx4 %0, %1, off sc1\n\ts_nop 1" :: "v"(p), "v"(w) : "memory"); }
;     __device__ __forceinline__ bool operator()(f32x4 (&acc)[2][2][4][2], const pg8::Unit& u, int wr, int wc, int fr, int fq) const {
;     ...
;             for (int m = 0; m < 4; ++m) { const int row = row0 + ai * 128 + m * 16; float ss = 0.f;
; #pragma unroll
;                 for (int bj = 0; bj < 2; ++bj) { const size_t off = (size_t)row * DM + colb + bj * 128; const u32x4 xw = xin[m][bj];
;                     f32x4 a = {bf_lo(xw.x), bf_hi(xw.x), bf_lo(xw.y), bf_hi(xw.y)}, b = {bf_lo(xw.z), bf_hi(xw.z), bf_lo(xw.w), bf_hi(xw.w)};
;                     a += acc[ai][bj][m][0]; b += acc[ai][bj][m][1];
;                     ss += ((a[0] * a[0] + a[1] * a[1]) + (a[2] * a[2] + a[3] * a[3])) + ((b[0] * b[0] + b[1] * b[1]) + (b[2] * b[2] + b[3] * b[3]));
;                     { u32x4 w; w.x = cvt_pk_bf16(a[0], a[1]); w.y = cvt_pk_bf16(a[2], a[3]); w.z = cvt_pk_bf16(b[0], b[1]); w.w = cvt_pk_bf16(b[2], b[3]); st16_wt(xb + off, w); } }
;                 ss += swz_xor<16>(ss); ss = half_sum(ss);
;                 if (fq == 0) xch[(ai * 128 + wr * 64 + m * 16 + fr) * 4 + wc] = ss; } }
	v_add_f32_e32 v48, v58, v48
	v_mov_b32_e32 v49, v48
	s_nop 1
	v_permlane32_swap_b32_e32 v48, v49
	s_and_saveexec_b64 s[4:5], s[10:11]
	v_add_f32_e32 v48, v48, v49
	ds_write_b32 v186, v48 offset:2048
	s_or_b64 exec, exec, s[4:5]
	v_lshlrev_b32_e32 v48, 16, v208
	v_and_b32_e32 v49, 0xffff0000, v208
	v_lshlrev_b32_e32 v50, 16, v209
	v_and_b32_e32 v51, 0xffff0000, v209
	v_lshlrev_b32_e32 v52, 16, v210
	v_and_b32_e32 v53, 0xffff0000, v210
	v_lshlrev_b32_e32 v54, 16, v211
	v_and_b32_e32 v55, 0xffff0000, v211
	v_pk_add_f32 v[46:47], v[46:47], v[50:51]
	v_pk_add_f32 v[44:45], v[44:45], v[48:49]
	v_pk_add_f32 v[48:49], v[42:43], v[54:55]
	v_pk_add_f32 v[42:43], v[40:41], v[52:53]
	v_mul_f32_e32 v40, v45, v45
	v_mul_f32_e32 v41, v47, v47
	v_fmac_f32_e32 v40, v44, v44
	v_fmac_f32_e32 v41, v46, v46
	v_add_f32_e32 v40, v40, v41
	v_mul_f32_e32 v41, v43, v43
	v_mul_f32_e32 v50, v49, v49
	v_fmac_f32_e32 v41, v42, v42
	v_fmac_f32_e32 v50, v48, v48
	v_readlane_b32 s2, v252, 8
	v_add_f32_e32 v41, v41, v50
	v_readlane_b32 s3, v252, 9
	v_add_f32_e32 v50, v40, v41
	v_cvt_pk_bf16_f32 v40, v44, v45
	v_cvt_pk_bf16_f32 v41, v46, v47
	v_cvt_pk_bf16_f32 v42, v42, v43
	v_cvt_pk_bf16_f32 v43, v48, v49
	s_nop 0
	v_lshl_add_u64 v[44:45], s[2:3], 0, v[92:93]
	v_lshl_add_u64 v[44:45], v[164:165], 1, v[44:45]
	global_store_dwordx4 v[44:45], v[40:43], off sc1
	s_nop 1
	v_lshlrev_b32_e32 v40, 16, v216
	v_and_b32_e32 v41, 0xffff0000, v216
	v_lshlrev_b32_e32 v42, 16, v217
	v_and_b32_e32 v43, 0xffff0000, v217
	v_lshlrev_b32_e32 v46, 16, v218
	v_and_b32_e32 v47, 0xffff0000, v218
	v_lshlrev_b32_e32 v48, 16, v219
	v_and_b32_e32 v49, 0xffff0000, v219
	v_pk_add_f32 v[38:39], v[38:39], v[42:43]
	v_pk_add_f32 v[36:37], v[36:37], v[40:41]
	v_pk_add_f32 v[40:41], v[34:35], v[48:49]
	v_pk_add_f32 v[34:35], v[32:33], v[46:47]
	v_mul_f32_e32 v32, v37, v37
	v_mul_f32_e32 v33, v39, v39
	v_fmac_f32_e32 v32, v36, v36
	v_fmac_f32_e32 v33, v38, v38
	v_add_f32_e32 v32, v32, v33
	v_mul_f32_e32 v33, v35, v35
	v_mul_f32_e32 v42, v41, v41
	v_fmac_f32_e32 v33, v34, v34
	v_fmac_f32_e32 v42, v40, v40
	v_add_f32_e32 v33, v33, v42
	v_add_f32_e32 v32, v32, v33
	v_add_f32_e32 v42, v50, v32
	v_cvt_pk_bf16_f32 v32, v36, v37
	v_cvt_pk_bf16_f32 v33, v38, v39
	ds_swizzle_b32 v38, v42 offset:swizzle(SWAP,16)
	s_mov_b64 s[2:3], 0x100
	v_cvt_pk_bf16_f32 v34, v34, v35
	v_cvt_pk_bf16_f32 v35, v40, v41
	v_lshl_add_u64 v[36:37], v[44:45], 0, s[2:3]
	global_store_dwordx4 v[36:37], v[32:35], off sc1
	s_nop 1
	s_waitcnt lgkmcnt(0)
	v_add_f32_e32 v32, v42, v38
	v_mov_b32_e32 v33, v32
	s_nop 1
	v_permlane32_swap_b32_e32 v32, v33
	s_and_saveexec_b64 s[4:5], s[10:11]
	v_add_f32_e32 v32, v32, v33
	ds_write_b32 v186, v32 offset:2304
	s_or_b64 exec, exec, s[4:5]
	v_lshlrev_b32_e32 v32, 16, v220
	v_and_b32_e32 v33, 0xffff0000, v220
	v_lshlrev_b32_e32 v34, 16, v221
	v_and_b32_e32 v35, 0xffff0000, v221
	v_lshlrev_b32_e32 v36, 16, v222
	v_and_b32_e32 v37, 0xffff0000, v222
	v_lshlrev_b32_e32 v38, 16, v223
	v_and_b32_e32 v39, 0xffff0000, v223
	v_pk_add_f32 v[30:31], v[30:31], v[34:35]
	v_pk_add_f32 v[28:29], v[28:29], v[32:33]
	v_pk_add_f32 v[32:33], v[26:27], v[38:39]
	v_pk_add_f32 v[26:27], v[24:25], v[36:37]
	v_mul_f32_e32 v24, v29, v29
	v_mul_f32_e32 v25, v31, v31
	v_fmac_f32_e32 v24, v28, v28
	v_fmac_f32_e32 v25, v30, v30
	v_add_f32_e32 v24, v24, v25
	v_mul_f32_e32 v25, v27, v27
	v_mul_f32_e32 v34, v33, v33
	v_fmac_f32_e32 v25, v26, v26
	v_fmac_f32_e32 v34, v32, v32
	v_readlane_b32 s2, v252, 8
	v_add_f32_e32 v25, v25, v34
	v_readlane_b32 s3, v252, 9
	v_add_f32_e32 v34, v24, v25
	v_cvt_pk_bf16_f32 v24, v28, v29
	v_cvt_pk_bf16_f32 v25, v30, v31
	v_cvt_pk_bf16_f32 v26, v26, v27
	v_cvt_pk_bf16_f32 v27, v32, v33
	s_nop 0
	v_lshl_add_u64 v[28:29], s[2:3], 0, v[90:91]
	v_lshl_add_u64 v[28:29], v[164:165], 1, v[28:29]
	global_store_dwordx4 v[28:29], v[24:27], off sc1
	s_nop 1
	v_lshlrev_b32_e32 v24, 16, v224
	v_and_b32_e32 v25, 0xffff0000, v224
	v_lshlrev_b32_e32 v26, 16, v225
	v_and_b32_e32 v27, 0xffff0000, v225
	v_lshlrev_b32_e32 v30, 16, v226
	v_and_b32_e32 v31, 0xffff0000, v226
	v_lshlrev_b32_e32 v32, 16, v227
	v_and_b32_e32 v33, 0xffff0000, v227
	v_pk_add_f32 v[22:23], v[22:23], v[26:27]
	v_pk_add_f32 v[20:21], v[20:21], v[24:25]
	v_pk_add_f32 v[24:25], v[18:19], v[32:33]
	v_pk_add_f32 v[18:19], v[16:17], v[30:31]
	v_mul_f32_e32 v16, v21, v21
	v_mul_f32_e32 v17, v23, v23
	v_fmac_f32_e32 v16, v20, v20
	v_fmac_f32_e32 v17, v22, v22
	v_add_f32_e32 v16, v16, v17
	v_mul_f32_e32 v17, v19, v19
	v_mul_f32_e32 v26, v25, v25
	v_fmac_f32_e32 v17, v18, v18
	v_fmac_f32_e32 v26, v24, v24
	v_add_f32_e32 v17, v17, v26
	v_add_f32_e32 v16, v16, v17
	v_add_f32_e32 v26, v34, v16
	v_cvt_pk_bf16_f32 v16, v20, v21
	v_cvt_pk_bf16_f32 v17, v22, v23
	ds_swizzle_b32 v22, v26 offset:swizzle(SWAP,16)
	s_mov_b64 s[2:3], 0x100
	v_cvt_pk_bf16_f32 v18, v18, v19
	v_cvt_pk_bf16_f32 v19, v24, v25
	v_lshl_add_u64 v[20:21], v[28:29], 0, s[2:3]
	global_store_dwordx4 v[20:21], v[16:19], off sc1
	s_nop 1
	s_waitcnt lgkmcnt(0)
; #define LAS __attribute__((address_space(3)))
; __device__ __forceinline__ unsigned cvt_pk_bf16(float lo, float hi) { unsigned r; asm volatile("v_cvt_pk_bf16_f32 %0, %1, %2" : "=v"(r) : "v"(lo), "v"(hi)); return r; }
; __device__ __forceinline__ float bf_lo(unsigned w) { return __uint_as_float(w << 16); }
; __device__ __forceinline__ float bf_hi(unsigned w) { return __uint_as_float(w & 0xffff0000u); }
; template <int M> __device__ __forceinline__ float swz_xor(float v) { return __int_as_float(__builtin_amdgcn_ds_swizzle(__float_as_int(v), (M << 10) | 0x1f)); }
; __device__ __forceinline__ float half_sum(float v) { auto rr = __builtin_amdgcn_permlane32_swap(__float_as_uint(v), __float_as_uint(v), false, false); return __uint_as_float(rr[0]) + __uint_as_float(rr[1]); }
; __device__ __forceinline__ void st16_wt(void* p, u32x4 w) { asm volatile("global_store_dwordx4 %0, %1, off sc1\n\ts_nop 1" :: "v"(p), "v"(w) : "memory"); }
;     __device__ __forceinline__ bool operator()(f32x4 (&acc)[2][2][4][2], const pg8::Unit& u, int wr, int wc, int fr, int fq) const {
;     ...
;             for (int m = 0; m < 4; ++m) { const int row = row0 + ai * 128 + m * 16; float ss = 0.f;
; #pragma unroll
;                 for (int bj = 0; bj < 2; ++bj) { const size_t off = (size_t)row * DM + colb + bj * 128; const u32x4 xw = xin[m][bj];
;                     f32x4 a = {bf_lo(xw.x), bf_hi(xw.x), bf_lo(xw.y), bf_hi(xw.y)}, b = {bf_lo(xw.z), bf_hi(xw.z), bf_lo(xw.w), bf_hi(xw.w)};
;                     a += acc[ai][bj][m][0]; b += acc[ai][bj][m][1];
;                     ss += ((a[0] * a[0] + a[1] * a[1]) + (a[2] * a[2] + a[3] * a[3])) + ((b[0] * b[0] + b[1] * b[1]) + (b[2] * b[2] + b[3] * b[3]));
;                     { u32x4 w; w.x = cvt_pk_bf16(a[0], a[1]); w.y = cvt_pk_bf16(a[2], a[3]); w.z = cvt_pk_bf16(b[0], b[1]); w.w = cvt_pk_bf16(b[2], b[3]); st16_wt(xb + off, w); } }
;                 ss += swz_xor<16>(ss); ss = half_sum(ss);
;                 if (fq == 0) xch[(ai * 128 + wr * 64 + m * 16 + fr) * 4 + wc] = ss; } }
;         asm volatile("s_waitcnt lgkmcnt(0)" ::: "memory"); __builtin_amdgcn_s_barrier(); asm volatile("" ::: "memory");
;         const int tid_ = (wr * 4 + wc) * 64 + fq * 16 + fr;
;         if (tid_ < 256) st16f_wt(part + (size_t)(u.pm * 256 + tid_) * 16 + u.pn * 4, *(const LAS f32x4*)(xch + tid_ * 4));
;         wave_arrive(done + 64 * u.pm, (fr | fq) == 0);
	v_add_f32_e32 v16, v26, v22
	v_mov_b32_e32 v17, v16
	s_nop 1
	v_permlane32_swap_b32_e32 v16, v17
	s_and_saveexec_b64 s[4:5], s[10:11]
	v_add_f32_e32 v16, v16, v17
	ds_write_b32 v186, v16 offset:2560
	s_or_b64 exec, exec, s[4:5]
	v_lshlrev_b32_e32 v16, 16, v240
	v_and_b32_e32 v17, 0xffff0000, v240
	v_lshlrev_b32_e32 v18, 16, v241
	v_and_b32_e32 v19, 0xffff0000, v241
	v_lshlrev_b32_e32 v20, 16, v242
	v_and_b32_e32 v21, 0xffff0000, v242
	v_lshlrev_b32_e32 v22, 16, v243
	v_and_b32_e32 v23, 0xffff0000, v243
	v_pk_add_f32 v[14:15], v[14:15], v[18:19]
	v_pk_add_f32 v[12:13], v[12:13], v[16:17]
	v_pk_add_f32 v[16:17], v[10:11], v[22:23]
	v_pk_add_f32 v[10:11], v[8:9], v[20:21]
	v_mul_f32_e32 v8, v13, v13
	v_mul_f32_e32 v9, v15, v15
	v_fmac_f32_e32 v8, v12, v12
	v_fmac_f32_e32 v9, v14, v14
	v_add_f32_e32 v8, v8, v9
	v_mul_f32_e32 v9, v11, v11
	v_mul_f32_e32 v18, v17, v17
	v_fmac_f32_e32 v9, v10, v10
	v_fmac_f32_e32 v18, v16, v16
	v_readlane_b32 s2, v252, 8
	v_add_f32_e32 v9, v9, v18
	v_readlane_b32 s3, v252, 9
	v_add_f32_e32 v18, v8, v9
	v_cvt_pk_bf16_f32 v8, v12, v13
	v_cvt_pk_bf16_f32 v9, v14, v15
	v_cvt_pk_bf16_f32 v10, v10, v11
	v_cvt_pk_bf16_f32 v11, v16, v17
	s_nop 0
	v_lshl_add_u64 v[12:13], s[2:3], 0, v[88:89]
	v_lshl_add_u64 v[12:13], v[164:165], 1, v[12:13]
	global_store_dwordx4 v[12:13], v[8:11], off sc1
	s_nop 1
	v_lshlrev_b32_e32 v8, 16, v244
	v_and_b32_e32 v9, 0xffff0000, v244
	v_lshlrev_b32_e32 v10, 16, v245
	v_and_b32_e32 v11, 0xffff0000, v245
	v_lshlrev_b32_e32 v14, 16, v246
	v_and_b32_e32 v15, 0xffff0000, v246
	v_lshlrev_b32_e32 v16, 16, v247
	v_and_b32_e32 v17, 0xffff0000, v247
	v_pk_add_f32 v[6:7], v[6:7], v[10:11]
	v_pk_add_f32 v[4:5], v[4:5], v[8:9]
	v_pk_add_f32 v[8:9], v[2:3], v[16:17]
	v_pk_add_f32 v[2:3], v[0:1], v[14:15]
	v_mul_f32_e32 v0, v5, v5
	v_mul_f32_e32 v1, v7, v7
	v_fmac_f32_e32 v0, v4, v4
	v_fmac_f32_e32 v1, v6, v6
	v_add_f32_e32 v0, v0, v1
	v_mul_f32_e32 v1, v3, v3
	v_mul_f32_e32 v10, v9, v9
	v_fmac_f32_e32 v1, v2, v2
	v_fmac_f32_e32 v10, v8, v8
	v_add_f32_e32 v1, v1, v10
	v_add_f32_e32 v0, v0, v1
	v_add_f32_e32 v10, v18, v0
	v_cvt_pk_bf16_f32 v0, v4, v5
	v_cvt_pk_bf16_f32 v1, v6, v7
	ds_swizzle_b32 v6, v10 offset:swizzle(SWAP,16)
	s_mov_b64 s[2:3], 0x100
	v_cvt_pk_bf16_f32 v2, v2, v3
	v_cvt_pk_bf16_f32 v3, v8, v9
	v_lshl_add_u64 v[4:5], v[12:13], 0, s[2:3]
	global_store_dwordx4 v[4:5], v[0:3], off sc1
	s_nop 1
	s_waitcnt lgkmcnt(0)
	v_add_f32_e32 v0, v10, v6
	v_mov_b32_e32 v1, v0
	s_nop 1
	v_permlane32_swap_b32_e32 v0, v1
	s_and_saveexec_b64 s[4:5], s[10:11]
	v_add_f32_e32 v0, v0, v1
	ds_write_b32 v186, v0 offset:2816
	s_or_b64 exec, exec, s[4:5]
	s_waitcnt lgkmcnt(0)
	s_barrier
	s_and_saveexec_b64 s[4:5], s[12:13]
	s_cbranch_execz .LBB0_1049
	v_add_u32_e32 v0, s7, v182
	v_ashrrev_i32_e32 v1, 31, v0
	v_readlane_b32 s2, v251, 32
	v_lshlrev_b64 v[0:1], 6, v[0:1]
	v_readlane_b32 s3, v251, 33
	s_nop 1
	v_lshl_add_u64 v[0:1], s[2:3], 0, v[0:1]
	s_lshl_b32 s2, s45, 2
	s_ashr_i32 s3, s2, 31
	v_lshl_add_u64 v[4:5], s[2:3], 2, v[0:1]
	ds_read_b128 v[0:3], v185
	s_waitcnt lgkmcnt(0)
	global_store_dwordx4 v[4:5], v[0:3], off sc1
	s_nop 1

; __device__ __forceinline__ unsigned cvt_pk_bf16(float lo, float hi) { unsigned r; asm volatile("v_cvt_pk_bf16_f32 %0, %1, %2" : "=v"(r) : "v"(lo), "v"(hi)); return r; }
; __device__ __forceinline__ float bf_lo(unsigned w) { return __uint_as_float(w << 16); }
; __device__ __forceinline__ float bf_hi(unsigned w) { return __uint_as_float(w & 0xffff0000u); }
; template <int M> __device__ __forceinline__ float swz_xor(float v) { return __int_as_float(__builtin_amdgcn_ds_swizzle(__float_as_int(v), (M << 10) | 0x1f)); }
; __device__ __forceinline__ float half_sum(float v) { auto rr = __builtin_amdgcn_permlane32_swap(__float_as_uint(v), __float_as_uint(v), false, false); return __uint_as_float(rr[0]) + __uint_as_float(rr[1]); }
; __device__ __forceinline__ void st16_wt(void* p, u32x4 w) { asm volatile("global_store_dwordx4 %0, %1, off sc1\n\ts_nop 1" :: "v"(p), "v"(w) : "memory"); }
;     __device__ __forceinline__ bool operator()(f32x4 (&acc)[2][2][4][2], const pg8::Unit& u, int wr, int wc, int fr, int fq) const {
;         const int row0 = u.pm * 256 + wr * 64 + fr, colb = u.pn * 256 + wc * 32 + 8 * fq;
; #pragma unroll
;         for (int ai = 0; ai < 2; ++ai) {
;             u32x4 xin[4][2];
; #pragma unroll
;             for (int m = 0; m < 4; ++m)
; #pragma unroll
;                 for (int bj = 0; bj < 2; ++bj) xin[m][bj] = *(const u32x4*)(xbase + (size_t)(row0 + ai * 128 + m * 16) * DM + colb + bj * 128);
; #pragma unroll
;             for (int m = 0; m < 4; ++m) { const int row = row0 + ai * 128 + m * 16; float ss = 0.f;
; #pragma unroll
;                 for (int bj = 0; bj < 2; ++bj) { const size_t off = (size_t)row * DM + colb + bj * 128; const u32x4 xw = xin[m][bj];
;                     f32x4 a = {bf_lo(xw.x), bf_hi(xw.x), bf_lo(xw.y), bf_hi(xw.y)}, b = {bf_lo(xw.z), bf_hi(xw.z), bf_lo(xw.w), bf_hi(xw.w)};
;                     a += acc[ai][bj][m][0]; b += acc[ai][bj][m][1];
;                     ss += ((a[0] * a[0] + a[1] * a[1]) + (a[2] * a[2] + a[3] * a[3])) + ((b[0] * b[0] + b[1] * b[1]) + (b[2] * b[2] + b[3] * b[3]));
;                     { u32x4 w; w.x = cvt_pk_bf16(a[0], a[1]); w.y = cvt_pk_bf16(a[2], a[3]); w.z = cvt_pk_bf16(b[0], b[1]); w.w = cvt_pk_bf16(b[2], b[3]); st16_wt(xb + off, w); } }
;                 ss += swz_xor<16>(ss); ss = half_sum(ss);
;                 if (fq == 0) xch[(ai * 128 + wr * 64 + m * 16 + fr) * 4 + wc] = ss; } }
.LBB0_1219:
	s_lshl_b32 s5, s40, 8
	v_lshl_or_b32 v164, s41, 8, v183
	v_add_u32_e32 v168, s5, v180
	v_ashrrev_i32_e32 v165, 31, v164
	v_readlane_b32 s2, v252, 8
	v_lshlrev_b64 v[176:177], 1, v[164:165]
	v_readlane_b32 s3, v252, 9
	v_ashrrev_i32_e32 v169, 31, v168
	v_lshlrev_b64 v[178:179], 11, v[168:169]
	v_lshl_add_u64 v[166:167], s[2:3], 0, v[176:177]
	v_lshl_add_u64 v[128:129], v[166:167], 0, v[178:179]
	global_load_dwordx4 v[196:199], v[128:129], off
	global_load_dwordx4 v[152:155], v[128:129], off offset:256
	v_or_b32_e32 v128, 16, v168
	v_ashrrev_i32_e32 v129, 31, v128
	v_lshlrev_b64 v[174:175], 11, v[128:129]
	v_lshl_add_u64 v[128:129], v[166:167], 0, v[174:175]
	global_load_dwordx4 v[148:151], v[128:129], off
	global_load_dwordx4 v[144:147], v[128:129], off offset:256
	v_or_b32_e32 v128, 32, v168
	v_ashrrev_i32_e32 v129, 31, v128
	v_lshlrev_b64 v[172:173], 11, v[128:129]
	v_lshl_add_u64 v[128:129], v[166:167], 0, v[172:173]
	global_load_dwordx4 v[140:143], v[128:129], off
	global_load_dwordx4 v[136:139], v[128:129], off offset:256
	v_or_b32_e32 v128, 48, v168
	v_ashrrev_i32_e32 v129, 31, v128
	v_lshlrev_b64 v[170:171], 11, v[128:129]
	v_lshl_add_u64 v[128:129], v[166:167], 0, v[170:171]
	global_load_dwordx4 v[132:135], v[128:129], off
	s_nop 0
	global_load_dwordx4 v[128:131], v[128:129], off offset:256
	v_lshlrev_b32_e32 v232, 11, v168
	v_mov_b32_e32 v233, 0
	v_add_u32_e32 v232, 0x40000, v232
	v_lshl_add_u64 v[234:235], v[166:167], 0, v[232:233]
	global_load_dwordx4 v[200:203], v[234:235], off
	global_load_dwordx4 v[204:207], v[234:235], off offset:256
	v_add_u32_e32 v232, 0x8000, v232
	v_lshl_add_u64 v[234:235], v[166:167], 0, v[232:233]
	global_load_dwordx4 v[208:211], v[234:235], off
	global_load_dwordx4 v[216:219], v[234:235], off offset:256
	v_add_u32_e32 v232, 0x8000, v232
	v_lshl_add_u64 v[234:235], v[166:167], 0, v[232:233]
	global_load_dwordx4 v[220:223], v[234:235], off
	global_load_dwordx4 v[224:227], v[234:235], off offset:256
	v_add_u32_e32 v232, 0x8000, v232
	v_lshl_add_u64 v[234:235], v[166:167], 0, v[232:233]
	global_load_dwordx4 v[240:243], v[234:235], off
	global_load_dwordx4 v[244:247], v[234:235], off offset:256
	s_waitcnt vmcnt(0)
	v_lshlrev_b32_e32 v188, 16, v196
	v_and_b32_e32 v189, 0xffff0000, v196
	v_lshlrev_b32_e32 v190, 16, v197
	v_and_b32_e32 v191, 0xffff0000, v197
	v_lshlrev_b32_e32 v192, 16, v198
	v_and_b32_e32 v193, 0xffff0000, v198
	v_lshlrev_b32_e32 v196, 16, v199
	v_and_b32_e32 v197, 0xffff0000, v199
	v_pk_add_f32 v[126:127], v[126:127], v[190:191]
	v_pk_add_f32 v[124:125], v[124:125], v[188:189]
	v_pk_add_f32 v[188:189], v[122:123], v[196:197]
	v_pk_add_f32 v[122:123], v[120:121], v[192:193]
	v_mul_f32_e32 v120, v125, v125
	v_mul_f32_e32 v121, v127, v127
	v_fmac_f32_e32 v120, v124, v124
	v_fmac_f32_e32 v121, v126, v126
	v_add_f32_e32 v120, v120, v121
	v_mul_f32_e32 v121, v123, v123
	v_mul_f32_e32 v187, v189, v189
	v_fmac_f32_e32 v121, v122, v122
	v_fmac_f32_e32 v187, v188, v188
	v_add_f32_e32 v121, v121, v187
	v_add_f32_e32 v187, v120, v121
	v_cvt_pk_bf16_f32 v120, v124, v125
	v_cvt_pk_bf16_f32 v121, v126, v127
	v_cvt_pk_bf16_f32 v122, v122, v123
	v_cvt_pk_bf16_f32 v123, v188, v189
	v_lshl_add_u64 v[124:125], s[2:3], 0, v[178:179]
	v_lshl_add_u64 v[124:125], v[124:125], 0, v[176:177]
	global_store_dwordx4 v[124:125], v[120:123], off sc1
	s_nop 1
	v_lshlrev_b32_e32 v120, 16, v152
	v_and_b32_e32 v121, 0xffff0000, v152
	v_lshlrev_b32_e32 v122, 16, v153
	v_and_b32_e32 v123, 0xffff0000, v153
	v_lshlrev_b32_e32 v126, 16, v154
	v_and_b32_e32 v127, 0xffff0000, v154
	v_lshlrev_b32_e32 v152, 16, v155
	v_and_b32_e32 v153, 0xffff0000, v155
	v_pk_add_f32 v[118:119], v[118:119], v[122:123]
	v_pk_add_f32 v[116:117], v[116:117], v[120:121]
	v_pk_add_f32 v[120:121], v[114:115], v[152:153]
	v_pk_add_f32 v[114:115], v[112:113], v[126:127]
	v_mul_f32_e32 v112, v117, v117
	v_mul_f32_e32 v113, v119, v119
	v_fmac_f32_e32 v112, v116, v116
	v_fmac_f32_e32 v113, v118, v118
	v_add_f32_e32 v112, v112, v113
	v_mul_f32_e32 v113, v115, v115
	v_mul_f32_e32 v122, v121, v121
	v_fmac_f32_e32 v113, v114, v114
	v_fmac_f32_e32 v122, v120, v120
	v_add_f32_e32 v113, v113, v122
	v_add_f32_e32 v112, v112, v113
	v_add_f32_e32 v122, v187, v112
	v_cvt_pk_bf16_f32 v112, v116, v117
	s_mov_b64 s[2:3], 0x100
	v_cvt_pk_bf16_f32 v113, v118, v119
	v_cvt_pk_bf16_f32 v114, v114, v115
	v_cvt_pk_bf16_f32 v115, v120, v121
	v_lshl_add_u64 v[116:117], v[124:125], 0, s[2:3]
	global_store_dwordx4 v[116:117], v[112:115], off sc1
	s_nop 1
	ds_swizzle_b32 v112, v122 offset:swizzle(SWAP,16)
	s_waitcnt lgkmcnt(0)
; __device__ __forceinline__ unsigned cvt_pk_bf16(float lo, float hi) { unsigned r; asm volatile("v_cvt_pk_bf16_f32 %0, %1, %2" : "=v"(r) : "v"(lo), "v"(hi)); return r; }
; __device__ __forceinline__ float bf_lo(unsigned w) { return __uint_as_float(w << 16); }
; __device__ __forceinline__ float bf_hi(unsigned w) { return __uint_as_float(w & 0xffff0000u); }
; template <int M> __device__ __forceinline__ float swz_xor(float v) { return __int_as_float(__builtin_amdgcn_ds_swizzle(__float_as_int(v), (M << 10) | 0x1f)); }
; __device__ __forceinline__ float half_sum(float v) { auto rr = __builtin_amdgcn_permlane32_swap(__float_as_uint(v), __float_as_uint(v), false, false); return __uint_as_float(rr[0]) + __uint_as_float(rr[1]); }
; __device__ __forceinline__ void st16_wt(void* p, u32x4 w) { asm volatile("global_store_dwordx4 %0, %1, off sc1\n\ts_nop 1" :: "v"(p), "v"(w) : "memory"); }
;     __device__ __forceinline__ bool operator()(f32x4 (&acc)[2][2][4][2], const pg8::Unit& u, int wr, int wc, int fr, int fq) const {
;     ...
;             for (int m = 0; m < 4; ++m) { const int row = row0 + ai * 128 + m * 16; float ss = 0.f;
; #pragma unroll
;                 for (int bj = 0; bj < 2; ++bj) { const size_t off = (size_t)row * DM + colb + bj * 128; const u32x4 xw = xin[m][bj];
;                     f32x4 a = {bf_lo(xw.x), bf_hi(xw.x), bf_lo(xw.y), bf_hi(xw.y)}, b = {bf_lo(xw.z), bf_hi(xw.z), bf_lo(xw.w), bf_hi(xw.w)};
;                     a += acc[ai][bj][m][0]; b += acc[ai][bj][m][1];
;                     ss += ((a[0] * a[0] + a[1] * a[1]) + (a[2] * a[2] + a[3] * a[3])) + ((b[0] * b[0] + b[1] * b[1]) + (b[2] * b[2] + b[3] * b[3]));
;                     { u32x4 w; w.x = cvt_pk_bf16(a[0], a[1]); w.y = cvt_pk_bf16(a[2], a[3]); w.z = cvt_pk_bf16(b[0], b[1]); w.w = cvt_pk_bf16(b[2], b[3]); st16_wt(xb + off, w); } }
;                 ss += swz_xor<16>(ss); ss = half_sum(ss);
;                 if (fq == 0) xch[(ai * 128 + wr * 64 + m * 16 + fr) * 4 + wc] = ss; } }
	v_add_f32_e32 v112, v122, v112
	v_mov_b32_e32 v113, v112
	s_nop 1
	v_permlane32_swap_b32_e32 v112, v113
	s_and_saveexec_b64 s[20:21], s[0:1]
	v_add_f32_e32 v112, v112, v113
	ds_write_b32 v186, v112
	s_or_b64 exec, exec, s[20:21]
	v_lshlrev_b32_e32 v112, 16, v148
	v_and_b32_e32 v113, 0xffff0000, v148
	v_lshlrev_b32_e32 v114, 16, v149
	v_and_b32_e32 v115, 0xffff0000, v149
	v_lshlrev_b32_e32 v116, 16, v150
	v_and_b32_e32 v117, 0xffff0000, v150
	v_lshlrev_b32_e32 v118, 16, v151
	v_and_b32_e32 v119, 0xffff0000, v151
	v_pk_add_f32 v[110:111], v[110:111], v[114:115]
	v_pk_add_f32 v[108:109], v[108:109], v[112:113]
	v_pk_add_f32 v[112:113], v[106:107], v[118:119]
	v_pk_add_f32 v[106:107], v[104:105], v[116:117]
	v_mul_f32_e32 v104, v109, v109
	v_mul_f32_e32 v105, v111, v111
	v_fmac_f32_e32 v104, v108, v108
	v_fmac_f32_e32 v105, v110, v110
	v_add_f32_e32 v104, v104, v105
	v_mul_f32_e32 v105, v107, v107
	v_mul_f32_e32 v114, v113, v113
	v_fmac_f32_e32 v105, v106, v106
	v_fmac_f32_e32 v114, v112, v112
	v_readlane_b32 s2, v252, 8
	v_add_f32_e32 v105, v105, v114
	v_readlane_b32 s3, v252, 9
	v_add_f32_e32 v114, v104, v105
	v_cvt_pk_bf16_f32 v104, v108, v109
	v_cvt_pk_bf16_f32 v105, v110, v111
	v_cvt_pk_bf16_f32 v106, v106, v107
	v_cvt_pk_bf16_f32 v107, v112, v113
	s_nop 0
	v_lshl_add_u64 v[108:109], s[2:3], 0, v[174:175]
	v_lshl_add_u64 v[108:109], v[164:165], 1, v[108:109]
	global_store_dwordx4 v[108:109], v[104:107], off sc1
	s_nop 1
	v_lshlrev_b32_e32 v104, 16, v144
	v_and_b32_e32 v105, 0xffff0000, v144
	v_lshlrev_b32_e32 v106, 16, v145
	v_and_b32_e32 v107, 0xffff0000, v145
	v_lshlrev_b32_e32 v110, 16, v146
	v_and_b32_e32 v111, 0xffff0000, v146
	v_lshlrev_b32_e32 v112, 16, v147
	v_and_b32_e32 v113, 0xffff0000, v147
	v_pk_add_f32 v[102:103], v[102:103], v[106:107]
	v_pk_add_f32 v[100:101], v[100:101], v[104:105]
	v_pk_add_f32 v[104:105], v[98:99], v[112:113]
	v_pk_add_f32 v[98:99], v[96:97], v[110:111]
	v_mul_f32_e32 v96, v101, v101
	v_mul_f32_e32 v97, v103, v103
	v_fmac_f32_e32 v96, v100, v100
	v_fmac_f32_e32 v97, v102, v102
	v_add_f32_e32 v96, v96, v97
	v_mul_f32_e32 v97, v99, v99
	v_mul_f32_e32 v106, v105, v105
	v_fmac_f32_e32 v97, v98, v98
	v_fmac_f32_e32 v106, v104, v104
	v_add_f32_e32 v97, v97, v106
	v_add_f32_e32 v96, v96, v97
	v_add_f32_e32 v106, v114, v96
	v_cvt_pk_bf16_f32 v96, v100, v101
	v_cvt_pk_bf16_f32 v97, v102, v103
	v_mov_b32_e32 v102, v106
	s_mov_b64 s[2:3], 0x100
	v_cvt_pk_bf16_f32 v98, v98, v99
	v_cvt_pk_bf16_f32 v99, v104, v105
	v_lshl_add_u64 v[100:101], v[108:109], 0, s[2:3]
	global_store_dwordx4 v[100:101], v[96:99], off sc1
	s_nop 1
	s_waitcnt lgkmcnt(0)
	s_nop 1
	v_permlane16_swap_b32_e32 v102, v106
	v_add_f32_e32 v96, v106, v102
	v_mov_b32_e32 v97, v96
	s_nop 1
	v_permlane32_swap_b32_e32 v96, v97
	s_and_saveexec_b64 s[20:21], s[0:1]
	v_add_f32_e32 v96, v96, v97
	ds_write_b32 v186, v96 offset:256
	s_or_b64 exec, exec, s[20:21]
	v_lshlrev_b32_e32 v96, 16, v140
	v_and_b32_e32 v97, 0xffff0000, v140
	v_lshlrev_b32_e32 v98, 16, v141
	v_and_b32_e32 v99, 0xffff0000, v141
	v_lshlrev_b32_e32 v100, 16, v142
	v_and_b32_e32 v101, 0xffff0000, v142
	v_lshlrev_b32_e32 v102, 16, v143
	v_and_b32_e32 v103, 0xffff0000, v143
	v_pk_add_f32 v[94:95], v[94:95], v[98:99]
	v_pk_add_f32 v[92:93], v[92:93], v[96:97]
	v_pk_add_f32 v[96:97], v[90:91], v[102:103]
	v_pk_add_f32 v[90:91], v[88:89], v[100:101]
	v_mul_f32_e32 v88, v93, v93
	v_mul_f32_e32 v89, v95, v95
	v_fmac_f32_e32 v88, v92, v92
	v_fmac_f32_e32 v89, v94, v94
	v_add_f32_e32 v88, v88, v89
	v_mul_f32_e32 v89, v91, v91
	v_mul_f32_e32 v98, v97, v97
	v_fmac_f32_e32 v89, v90, v90
	v_fmac_f32_e32 v98, v96, v96
	v_readlane_b32 s2, v252, 8
	v_add_f32_e32 v89, v89, v98
	v_readlane_b32 s3, v252, 9
	v_add_f32_e32 v98, v88, v89
	v_cvt_pk_bf16_f32 v88, v92, v93
	v_cvt_pk_bf16_f32 v89, v94, v95
	v_cvt_pk_bf16_f32 v90, v90, v91
	v_cvt_pk_bf16_f32 v91, v96, v97
	s_nop 0
	v_lshl_add_u64 v[92:93], s[2:3], 0, v[172:173]
	v_lshl_add_u64 v[92:93], v[164:165], 1, v[92:93]
	global_store_dwordx4 v[92:93], v[88:91], off sc1
	s_nop 1
	v_lshlrev_b32_e32 v88, 16, v136
	v_and_b32_e32 v89, 0xffff0000, v136
	v_lshlrev_b32_e32 v90, 16, v137
	v_and_b32_e32 v91, 0xffff0000, v137
	v_lshlrev_b32_e32 v94, 16, v138
	v_and_b32_e32 v95, 0xffff0000, v138
	v_lshlrev_b32_e32 v96, 16, v139
	v_and_b32_e32 v97, 0xffff0000, v139
	v_pk_add_f32 v[86:87], v[86:87], v[90:91]
	v_pk_add_f32 v[84:85], v[84:85], v[88:89]
	v_pk_add_f32 v[88:89], v[82:83], v[96:97]
	v_pk_add_f32 v[82:83], v[80:81], v[94:95]
	v_mul_f32_e32 v80, v85, v85
	v_mul_f32_e32 v81, v87, v87
	v_fmac_f32_e32 v80, v84, v84
	v_fmac_f32_e32 v81, v86, v86
	v_add_f32_e32 v80, v80, v81
	v_mul_f32_e32 v81, v83, v83
	v_mul_f32_e32 v90, v89, v89
	v_fmac_f32_e32 v81, v82, v82
	v_fmac_f32_e32 v90, v88, v88
	v_add_f32_e32 v81, v81, v90
	v_add_f32_e32 v80, v80, v81
	v_add_f32_e32 v90, v98, v80
	v_cvt_pk_bf16_f32 v80, v84, v85
	v_cvt_pk_bf16_f32 v81, v86, v87
	v_mov_b32_e32 v86, v90
	s_mov_b64 s[2:3], 0x100
	v_cvt_pk_bf16_f32 v82, v82, v83
	v_cvt_pk_bf16_f32 v83, v88, v89
	v_lshl_add_u64 v[84:85], v[92:93], 0, s[2:3]
	global_store_dwordx4 v[84:85], v[80:83], off sc1
	s_nop 1
	s_waitcnt lgkmcnt(0)
; __device__ __forceinline__ unsigned cvt_pk_bf16(float lo, float hi) { unsigned r; asm volatile("v_cvt_pk_bf16_f32 %0, %1, %2" : "=v"(r) : "v"(lo), "v"(hi)); return r; }
; __device__ __forceinline__ float bf_lo(unsigned w) { return __uint_as_float(w << 16); }
; __device__ __forceinline__ float bf_hi(unsigned w) { return __uint_as_float(w & 0xffff0000u); }
; template <int M> __device__ __forceinline__ float swz_xor(float v) { return __int_as_float(__builtin_amdgcn_ds_swizzle(__float_as_int(v), (M << 10) | 0x1f)); }
; __device__ __forceinline__ float half_sum(float v) { auto rr = __builtin_amdgcn_permlane32_swap(__float_as_uint(v), __float_as_uint(v), false, false); return __uint_as_float(rr[0]) + __uint_as_float(rr[1]); }
; __device__ __forceinline__ void st16_wt(void* p, u32x4 w) { asm volatile("global_store_dwordx4 %0, %1, off sc1\n\ts_nop 1" :: "v"(p), "v"(w) : "memory"); }
;     __device__ __forceinline__ bool operator()(f32x4 (&acc)[2][2][4][2], const pg8::Unit& u, int wr, int wc, int fr, int fq) const {
;     ...
;         for (int ai = 0; ai < 2; ++ai) {
;             u32x4 xin[4][2];
; #pragma unroll
;             for (int m = 0; m < 4; ++m)
; #pragma unroll
;                 for (int bj = 0; bj < 2; ++bj) xin[m][bj] = *(const u32x4*)(xbase + (size_t)(row0 + ai * 128 + m * 16) * DM + colb + bj * 128);
; #pragma unroll
;             for (int m = 0; m < 4; ++m) { const int row = row0 + ai * 128 + m * 16; float ss = 0.f;
; #pragma unroll
;                 for (int bj = 0; bj < 2; ++bj) { const size_t off = (size_t)row * DM + colb + bj * 128; const u32x4 xw = xin[m][bj];
;                     f32x4 a = {bf_lo(xw.x), bf_hi(xw.x), bf_lo(xw.y), bf_hi(xw.y)}, b = {bf_lo(xw.z), bf_hi(xw.z), bf_lo(xw.w), bf_hi(xw.w)};
;                     a += acc[ai][bj][m][0]; b += acc[ai][bj][m][1];
;                     ss += ((a[0] * a[0] + a[1] * a[1]) + (a[2] * a[2] + a[3] * a[3])) + ((b[0] * b[0] + b[1] * b[1]) + (b[2] * b[2] + b[3] * b[3]));
;                     { u32x4 w; w.x = cvt_pk_bf16(a[0], a[1]); w.y = cvt_pk_bf16(a[2], a[3]); w.z = cvt_pk_bf16(b[0], b[1]); w.w = cvt_pk_bf16(b[2], b[3]); st16_wt(xb + off, w); } }
;                 ss += swz_xor<16>(ss); ss = half_sum(ss);
;                 if (fq == 0) xch[(ai * 128 + wr * 64 + m * 16 + fr) * 4 + wc] = ss; } }
	s_nop 1
	v_permlane16_swap_b32_e32 v86, v90
	v_add_f32_e32 v80, v90, v86
	v_mov_b32_e32 v81, v80
	s_nop 1
	v_permlane32_swap_b32_e32 v80, v81
	s_and_saveexec_b64 s[20:21], s[0:1]
	v_add_f32_e32 v80, v80, v81
	ds_write_b32 v186, v80 offset:512
	s_or_b64 exec, exec, s[20:21]
	v_lshlrev_b32_e32 v80, 16, v132
	v_and_b32_e32 v81, 0xffff0000, v132
	v_lshlrev_b32_e32 v82, 16, v133
	v_and_b32_e32 v83, 0xffff0000, v133
	v_lshlrev_b32_e32 v84, 16, v134
	v_and_b32_e32 v85, 0xffff0000, v134
	v_lshlrev_b32_e32 v86, 16, v135
	v_and_b32_e32 v87, 0xffff0000, v135
	v_pk_add_f32 v[78:79], v[78:79], v[82:83]
	v_pk_add_f32 v[76:77], v[76:77], v[80:81]
	v_pk_add_f32 v[80:81], v[74:75], v[86:87]
	v_pk_add_f32 v[74:75], v[72:73], v[84:85]
	v_mul_f32_e32 v72, v77, v77
	v_mul_f32_e32 v73, v79, v79
	v_fmac_f32_e32 v72, v76, v76
	v_fmac_f32_e32 v73, v78, v78
	v_add_f32_e32 v72, v72, v73
	v_mul_f32_e32 v73, v75, v75
	v_mul_f32_e32 v82, v81, v81
	v_fmac_f32_e32 v73, v74, v74
	v_fmac_f32_e32 v82, v80, v80
	v_readlane_b32 s2, v252, 8
	v_add_f32_e32 v73, v73, v82
	v_readlane_b32 s3, v252, 9
	v_add_f32_e32 v82, v72, v73
	v_cvt_pk_bf16_f32 v72, v76, v77
	v_cvt_pk_bf16_f32 v73, v78, v79
	v_cvt_pk_bf16_f32 v74, v74, v75
	v_cvt_pk_bf16_f32 v75, v80, v81
	s_nop 0
	v_lshl_add_u64 v[76:77], s[2:3], 0, v[170:171]
	v_lshl_add_u64 v[76:77], v[164:165], 1, v[76:77]
	global_store_dwordx4 v[76:77], v[72:75], off sc1
	s_nop 1
	v_lshlrev_b32_e32 v72, 16, v128
	v_and_b32_e32 v73, 0xffff0000, v128
	v_lshlrev_b32_e32 v74, 16, v129
	v_and_b32_e32 v75, 0xffff0000, v129
	v_lshlrev_b32_e32 v78, 16, v130
	v_and_b32_e32 v79, 0xffff0000, v130
	v_lshlrev_b32_e32 v80, 16, v131
	v_and_b32_e32 v81, 0xffff0000, v131
	v_pk_add_f32 v[70:71], v[70:71], v[74:75]
	v_pk_add_f32 v[68:69], v[68:69], v[72:73]
	v_pk_add_f32 v[72:73], v[66:67], v[80:81]
	v_pk_add_f32 v[66:67], v[64:65], v[78:79]
	v_mul_f32_e32 v64, v69, v69
	v_mul_f32_e32 v65, v71, v71
	v_fmac_f32_e32 v64, v68, v68
	v_fmac_f32_e32 v65, v70, v70
	v_add_f32_e32 v64, v64, v65
	v_mul_f32_e32 v65, v67, v67
	v_mul_f32_e32 v74, v73, v73
	v_fmac_f32_e32 v65, v66, v66
	v_fmac_f32_e32 v74, v72, v72
	v_add_f32_e32 v65, v65, v74
	v_add_f32_e32 v64, v64, v65
	v_add_f32_e32 v74, v82, v64
	v_cvt_pk_bf16_f32 v64, v68, v69
	v_cvt_pk_bf16_f32 v65, v70, v71
	v_mov_b32_e32 v70, v74
	s_mov_b64 s[2:3], 0x100
	v_cvt_pk_bf16_f32 v66, v66, v67
	v_cvt_pk_bf16_f32 v67, v72, v73
	v_lshl_add_u64 v[68:69], v[76:77], 0, s[2:3]
	global_store_dwordx4 v[68:69], v[64:67], off sc1
	s_nop 1
	s_waitcnt lgkmcnt(0)
	s_nop 1
	v_permlane16_swap_b32_e32 v70, v74
	v_add_f32_e32 v64, v74, v70
	v_mov_b32_e32 v65, v64
	s_nop 1
	v_permlane32_swap_b32_e32 v64, v65
	s_and_saveexec_b64 s[20:21], s[0:1]
	v_add_f32_e32 v64, v64, v65
	ds_write_b32 v186, v64 offset:768
	s_or_b64 exec, exec, s[20:21]
	v_lshlrev_b64 v[64:65], 11, v[168:169]
	s_mov_b64 s[2:3], 0x40000
	v_lshl_add_u64 v[102:103], v[64:65], 0, s[2:3]
	v_lshl_add_u64 v[66:67], v[166:167], 0, v[102:103]
	s_mov_b64 s[2:3], 0x48000
	v_lshl_add_u64 v[92:93], v[64:65], 0, s[2:3]
	s_mov_b64 s[2:3], 0x50000
	v_lshl_add_u64 v[90:91], v[64:65], 0, s[2:3]
	s_mov_b64 s[2:3], 0x58000
	v_lshl_add_u64 v[66:67], v[166:167], 0, v[92:93]
	v_lshl_add_u64 v[88:89], v[64:65], 0, s[2:3]
	v_lshl_add_u64 v[66:67], v[166:167], 0, v[90:91]
	v_lshl_add_u64 v[64:65], v[166:167], 0, v[88:89]
	v_readlane_b32 s2, v252, 8
	v_readlane_b32 s3, v252, 9
	v_lshlrev_b32_e32 v104, 16, v200
	v_and_b32_e32 v105, 0xffff0000, v200
	v_lshlrev_b32_e32 v94, 16, v201
	v_and_b32_e32 v95, 0xffff0000, v201
	v_lshlrev_b32_e32 v106, 16, v202
	v_and_b32_e32 v107, 0xffff0000, v202
	v_lshlrev_b32_e32 v96, 16, v203
	v_and_b32_e32 v97, 0xffff0000, v203
	v_pk_add_f32 v[62:63], v[62:63], v[94:95]
	v_pk_add_f32 v[60:61], v[60:61], v[104:105]
	v_pk_add_f32 v[94:95], v[58:59], v[96:97]
	v_pk_add_f32 v[58:59], v[56:57], v[106:107]
	v_mul_f32_e32 v56, v61, v61
	v_mul_f32_e32 v57, v63, v63
	v_fmac_f32_e32 v56, v60, v60
	v_fmac_f32_e32 v57, v62, v62
	v_add_f32_e32 v56, v56, v57
	v_mul_f32_e32 v57, v59, v59
	v_mul_f32_e32 v96, v95, v95
	v_fmac_f32_e32 v57, v58, v58
	v_fmac_f32_e32 v96, v94, v94
	v_add_f32_e32 v57, v57, v96
	v_add_f32_e32 v96, v56, v57
	v_cvt_pk_bf16_f32 v56, v60, v61
	v_cvt_pk_bf16_f32 v57, v62, v63
	v_cvt_pk_bf16_f32 v58, v58, v59
	v_cvt_pk_bf16_f32 v59, v94, v95
	v_lshl_add_u64 v[60:61], s[2:3], 0, v[102:103]
	v_lshl_add_u64 v[60:61], v[164:165], 1, v[60:61]
	global_store_dwordx4 v[60:61], v[56:59], off sc1
	s_nop 1
	v_lshlrev_b32_e32 v56, 16, v204
	v_and_b32_e32 v57, 0xffff0000, v204
	v_lshlrev_b32_e32 v58, 16, v205
	v_and_b32_e32 v59, 0xffff0000, v205
	v_lshlrev_b32_e32 v62, 16, v206
	v_and_b32_e32 v63, 0xffff0000, v206
	v_lshlrev_b32_e32 v94, 16, v207
	v_and_b32_e32 v95, 0xffff0000, v207
	v_pk_add_f32 v[54:55], v[54:55], v[58:59]
	v_pk_add_f32 v[52:53], v[52:53], v[56:57]
	v_pk_add_f32 v[56:57], v[50:51], v[94:95]
	v_pk_add_f32 v[50:51], v[48:49], v[62:63]
	v_mul_f32_e32 v48, v53, v53
	v_mul_f32_e32 v49, v55, v55
	v_fmac_f32_e32 v48, v52, v52
	v_fmac_f32_e32 v49, v54, v54
	v_add_f32_e32 v48, v48, v49
	v_mul_f32_e32 v49, v51, v51
	v_mul_f32_e32 v58, v57, v57
	v_fmac_f32_e32 v49, v50, v50
	v_fmac_f32_e32 v58, v56, v56
	v_add_f32_e32 v49, v49, v58
	v_add_f32_e32 v48, v48, v49
	v_add_f32_e32 v58, v96, v48
	v_cvt_pk_bf16_f32 v48, v52, v53
	s_mov_b64 s[2:3], 0x100
	v_cvt_pk_bf16_f32 v49, v54, v55
	v_cvt_pk_bf16_f32 v50, v50, v51
	v_cvt_pk_bf16_f32 v51, v56, v57
	v_lshl_add_u64 v[52:53], v[60:61], 0, s[2:3]
	global_store_dwordx4 v[52:53], v[48:51], off sc1
	s_nop 1
	ds_swizzle_b32 v48, v58 offset:swizzle(SWAP,16)
	s_waitcnt lgkmcnt(0)
; __device__ __forceinline__ unsigned cvt_pk_bf16(float lo, float hi) { unsigned r; asm volatile("v_cvt_pk_bf16_f32 %0, %1, %2" : "=v"(r) : "v"(lo), "v"(hi)); return r; }
; __device__ __forceinline__ float bf_lo(unsigned w) { return __uint_as_float(w << 16); }
; __device__ __forceinline__ float bf_hi(unsigned w) { return __uint_as_float(w & 0xffff0000u); }
; template <int M> __device__ __forceinline__ float swz_xor(float v) { return __int_as_float(__builtin_amdgcn_ds_swizzle(__float_as_int(v), (M << 10) | 0x1f)); }
; __device__ __forceinline__ float half_sum(float v) { auto rr = __builtin_amdgcn_permlane32_swap(__float_as_uint(v), __float_as_uint(v), false, false); return __uint_as_float(rr[0]) + __uint_as_float(rr[1]); }
; __device__ __forceinline__ void st16_wt(void* p, u32x4 w) { asm volatile("global_store_dwordx4 %0, %1, off sc1\n\ts_nop 1" :: "v"(p), "v"(w) : "memory"); }
;     __device__ __forceinline__ bool operator()(f32x4 (&acc)[2][2][4][2], const pg8::Unit& u, int wr, int wc, int fr, int fq) const {
;     ...
;             for (int m = 0; m < 4; ++m) { const int row = row0 + ai * 128 + m * 16; float ss = 0.f;
; #pragma unroll
;                 for (int bj = 0; bj < 2; ++bj) { const size_t off = (size_t)row * DM + colb + bj * 128; const u32x4 xw = xin[m][bj];
;                     f32x4 a = {bf_lo(xw.x), bf_hi(xw.x), bf_lo(xw.y), bf_hi(xw.y)}, b = {bf_lo(xw.z), bf_hi(xw.z), bf_lo(xw.w), bf_hi(xw.w)};
;                     a += acc[ai][bj][m][0]; b += acc[ai][bj][m][1];
;                     ss += ((a[0] * a[0] + a[1] * a[1]) + (a[2] * a[2] + a[3] * a[3])) + ((b[0] * b[0] + b[1] * b[1]) + (b[2] * b[2] + b[3] * b[3]));
;                     { u32x4 w; w.x = cvt_pk_bf16(a[0], a[1]); w.y = cvt_pk_bf16(a[2], a[3]); w.z = cvt_pk_bf16(b[0], b[1]); w.w = cvt_pk_bf16(b[2], b[3]); st16_wt(xb + off, w); } }
;                 ss += swz_xor<16>(ss); ss = half_sum(ss);
;                 if (fq == 0) xch[(ai * 128 + wr * 64 + m * 16 + fr) * 4 + wc] = ss; } }
	v_add_f32_e32 v48, v58, v48
	v_mov_b32_e32 v49, v48
	s_nop 1
	v_permlane32_swap_b32_e32 v48, v49
	s_and_saveexec_b64 s[20:21], s[0:1]
	v_add_f32_e32 v48, v48, v49
	ds_write_b32 v186, v48 offset:2048
	s_or_b64 exec, exec, s[20:21]
	v_lshlrev_b32_e32 v48, 16, v208
	v_and_b32_e32 v49, 0xffff0000, v208
	v_lshlrev_b32_e32 v50, 16, v209
	v_and_b32_e32 v51, 0xffff0000, v209
	v_lshlrev_b32_e32 v52, 16, v210
	v_and_b32_e32 v53, 0xffff0000, v210
	v_lshlrev_b32_e32 v54, 16, v211
	v_and_b32_e32 v55, 0xffff0000, v211
	v_pk_add_f32 v[46:47], v[46:47], v[50:51]
	v_pk_add_f32 v[44:45], v[44:45], v[48:49]
	v_pk_add_f32 v[48:49], v[42:43], v[54:55]
	v_pk_add_f32 v[42:43], v[40:41], v[52:53]
	v_mul_f32_e32 v40, v45, v45
	v_mul_f32_e32 v41, v47, v47
	v_fmac_f32_e32 v40, v44, v44
	v_fmac_f32_e32 v41, v46, v46
	v_add_f32_e32 v40, v40, v41
	v_mul_f32_e32 v41, v43, v43
	v_mul_f32_e32 v50, v49, v49
	v_fmac_f32_e32 v41, v42, v42
	v_fmac_f32_e32 v50, v48, v48
	v_readlane_b32 s2, v252, 8
	v_add_f32_e32 v41, v41, v50
	v_readlane_b32 s3, v252, 9
	v_add_f32_e32 v50, v40, v41
	v_cvt_pk_bf16_f32 v40, v44, v45
	v_cvt_pk_bf16_f32 v41, v46, v47
	v_cvt_pk_bf16_f32 v42, v42, v43
	v_cvt_pk_bf16_f32 v43, v48, v49
	s_nop 0
	v_lshl_add_u64 v[44:45], s[2:3], 0, v[92:93]
	v_lshl_add_u64 v[44:45], v[164:165], 1, v[44:45]
	global_store_dwordx4 v[44:45], v[40:43], off sc1
	s_nop 1
	v_lshlrev_b32_e32 v40, 16, v216
	v_and_b32_e32 v41, 0xffff0000, v216
	v_lshlrev_b32_e32 v42, 16, v217
	v_and_b32_e32 v43, 0xffff0000, v217
	v_lshlrev_b32_e32 v46, 16, v218
	v_and_b32_e32 v47, 0xffff0000, v218
	v_lshlrev_b32_e32 v48, 16, v219
	v_and_b32_e32 v49, 0xffff0000, v219
	v_pk_add_f32 v[38:39], v[38:39], v[42:43]
	v_pk_add_f32 v[36:37], v[36:37], v[40:41]
	v_pk_add_f32 v[40:41], v[34:35], v[48:49]
	v_pk_add_f32 v[34:35], v[32:33], v[46:47]
	v_mul_f32_e32 v32, v37, v37
	v_mul_f32_e32 v33, v39, v39
	v_fmac_f32_e32 v32, v36, v36
	v_fmac_f32_e32 v33, v38, v38
	v_add_f32_e32 v32, v32, v33
	v_mul_f32_e32 v33, v35, v35
	v_mul_f32_e32 v42, v41, v41
	v_fmac_f32_e32 v33, v34, v34
	v_fmac_f32_e32 v42, v40, v40
	v_add_f32_e32 v33, v33, v42
	v_add_f32_e32 v32, v32, v33
	v_add_f32_e32 v42, v50, v32
	v_cvt_pk_bf16_f32 v32, v36, v37
	v_cvt_pk_bf16_f32 v33, v38, v39
	ds_swizzle_b32 v38, v42 offset:swizzle(SWAP,16)
	s_mov_b64 s[2:3], 0x100
	v_cvt_pk_bf16_f32 v34, v34, v35
	v_cvt_pk_bf16_f32 v35, v40, v41
	v_lshl_add_u64 v[36:37], v[44:45], 0, s[2:3]
	global_store_dwordx4 v[36:37], v[32:35], off sc1
	s_nop 1
	s_waitcnt lgkmcnt(0)
	v_add_f32_e32 v32, v42, v38
	v_mov_b32_e32 v33, v32
	s_nop 1
	v_permlane32_swap_b32_e32 v32, v33
	s_and_saveexec_b64 s[20:21], s[0:1]
	v_add_f32_e32 v32, v32, v33
	ds_write_b32 v186, v32 offset:2304
	s_or_b64 exec, exec, s[20:21]
	v_lshlrev_b32_e32 v32, 16, v220
	v_and_b32_e32 v33, 0xffff0000, v220
	v_lshlrev_b32_e32 v34, 16, v221
	v_and_b32_e32 v35, 0xffff0000, v221
	v_lshlrev_b32_e32 v36, 16, v222
	v_and_b32_e32 v37, 0xffff0000, v222
	v_lshlrev_b32_e32 v38, 16, v223
	v_and_b32_e32 v39, 0xffff0000, v223
	v_pk_add_f32 v[30:31], v[30:31], v[34:35]
	v_pk_add_f32 v[28:29], v[28:29], v[32:33]
	v_pk_add_f32 v[32:33], v[26:27], v[38:39]
	v_pk_add_f32 v[26:27], v[24:25], v[36:37]
	v_mul_f32_e32 v24, v29, v29
	v_mul_f32_e32 v25, v31, v31
	v_fmac_f32_e32 v24, v28, v28
	v_fmac_f32_e32 v25, v30, v30
	v_add_f32_e32 v24, v24, v25
	v_mul_f32_e32 v25, v27, v27
	v_mul_f32_e32 v34, v33, v33
	v_fmac_f32_e32 v25, v26, v26
	v_fmac_f32_e32 v34, v32, v32
	v_readlane_b32 s2, v252, 8
	v_add_f32_e32 v25, v25, v34
	v_readlane_b32 s3, v252, 9
	v_add_f32_e32 v34, v24, v25
	v_cvt_pk_bf16_f32 v24, v28, v29
	v_cvt_pk_bf16_f32 v25, v30, v31
	v_cvt_pk_bf16_f32 v26, v26, v27
	v_cvt_pk_bf16_f32 v27, v32, v33
	s_nop 0
	v_lshl_add_u64 v[28:29], s[2:3], 0, v[90:91]
	v_lshl_add_u64 v[28:29], v[164:165], 1, v[28:29]
	global_store_dwordx4 v[28:29], v[24:27], off sc1
	s_nop 1
	v_lshlrev_b32_e32 v24, 16, v224
	v_and_b32_e32 v25, 0xffff0000, v224
	v_lshlrev_b32_e32 v26, 16, v225
	v_and_b32_e32 v27, 0xffff0000, v225
	v_lshlrev_b32_e32 v30, 16, v226
	v_and_b32_e32 v31, 0xffff0000, v226
	v_lshlrev_b32_e32 v32, 16, v227
	v_and_b32_e32 v33, 0xffff0000, v227
	v_pk_add_f32 v[22:23], v[22:23], v[26:27]
	v_pk_add_f32 v[20:21], v[20:21], v[24:25]
	v_pk_add_f32 v[24:25], v[18:19], v[32:33]
	v_pk_add_f32 v[18:19], v[16:17], v[30:31]
	v_mul_f32_e32 v16, v21, v21
	v_mul_f32_e32 v17, v23, v23
	v_fmac_f32_e32 v16, v20, v20
	v_fmac_f32_e32 v17, v22, v22
	v_add_f32_e32 v16, v16, v17
	v_mul_f32_e32 v17, v19, v19
	v_mul_f32_e32 v26, v25, v25
	v_fmac_f32_e32 v17, v18, v18
	v_fmac_f32_e32 v26, v24, v24
	v_add_f32_e32 v17, v17, v26
	v_add_f32_e32 v16, v16, v17
	v_add_f32_e32 v26, v34, v16
	v_cvt_pk_bf16_f32 v16, v20, v21
	v_cvt_pk_bf16_f32 v17, v22, v23
	ds_swizzle_b32 v22, v26 offset:swizzle(SWAP,16)
	s_mov_b64 s[2:3], 0x100
	v_cvt_pk_bf16_f32 v18, v18, v19
	v_cvt_pk_bf16_f32 v19, v24, v25
	v_lshl_add_u64 v[20:21], v[28:29], 0, s[2:3]
	global_store_dwordx4 v[20:21], v[16:19], off sc1
	s_nop 1
	s_waitcnt lgkmcnt(0)
; #define LAS __attribute__((address_space(3)))
; __device__ __forceinline__ unsigned cvt_pk_bf16(float lo, float hi) { unsigned r; asm volatile("v_cvt_pk_bf16_f32 %0, %1, %2" : "=v"(r) : "v"(lo), "v"(hi)); return r; }
; __device__ __forceinline__ float bf_lo(unsigned w) { return __uint_as_float(w << 16); }
; __device__ __forceinline__ float bf_hi(unsigned w) { return __uint_as_float(w & 0xffff0000u); }
; template <int M> __device__ __forceinline__ float swz_xor(float v) { return __int_as_float(__builtin_amdgcn_ds_swizzle(__float_as_int(v), (M << 10) | 0x1f)); }
; __device__ __forceinline__ float half_sum(float v) { auto rr = __builtin_amdgcn_permlane32_swap(__float_as_uint(v), __float_as_uint(v), false, false); return __uint_as_float(rr[0]) + __uint_as_float(rr[1]); }
; __device__ __forceinline__ void st16_wt(void* p, u32x4 w) { asm volatile("global_store_dwordx4 %0, %1, off sc1\n\ts_nop 1" :: "v"(p), "v"(w) : "memory"); }
;     __device__ __forceinline__ bool operator()(f32x4 (&acc)[2][2][4][2], const pg8::Unit& u, int wr, int wc, int fr, int fq) const {
;     ...
;             for (int m = 0; m < 4; ++m) { const int row = row0 + ai * 128 + m * 16; float ss = 0.f;
; #pragma unroll
;                 for (int bj = 0; bj < 2; ++bj) { const size_t off = (size_t)row * DM + colb + bj * 128; const u32x4 xw = xin[m][bj];
;                     f32x4 a = {bf_lo(xw.x), bf_hi(xw.x), bf_lo(xw.y), bf_hi(xw.y)}, b = {bf_lo(xw.z), bf_hi(xw.z), bf_lo(xw.w), bf_hi(xw.w)};
;                     a += acc[ai][bj][m][0]; b += acc[ai][bj][m][1];
;                     ss += ((a[0] * a[0] + a[1] * a[1]) + (a[2] * a[2] + a[3] * a[3])) + ((b[0] * b[0] + b[1] * b[1]) + (b[2] * b[2] + b[3] * b[3]));
;                     { u32x4 w; w.x = cvt_pk_bf16(a[0], a[1]); w.y = cvt_pk_bf16(a[2], a[3]); w.z = cvt_pk_bf16(b[0], b[1]); w.w = cvt_pk_bf16(b[2], b[3]); st16_wt(xb + off, w); } }
;                 ss += swz_xor<16>(ss); ss = half_sum(ss);
;                 if (fq == 0) xch[(ai * 128 + wr * 64 + m * 16 + fr) * 4 + wc] = ss; } }
;         asm volatile("s_waitcnt lgkmcnt(0)" ::: "memory"); __builtin_amdgcn_s_barrier(); asm volatile("" ::: "memory");
;         const int tid_ = (wr * 4 + wc) * 64 + fq * 16 + fr;
;         if (tid_ < 256) st16f_wt(part + (size_t)(u.pm * 256 + tid_) * 16 + u.pn * 4, *(const LAS f32x4*)(xch + tid_ * 4));
	v_add_f32_e32 v16, v26, v22
	v_mov_b32_e32 v17, v16
	s_nop 1
	v_permlane32_swap_b32_e32 v16, v17
	s_and_saveexec_b64 s[20:21], s[0:1]
	v_add_f32_e32 v16, v16, v17
	ds_write_b32 v186, v16 offset:2560
	s_or_b64 exec, exec, s[20:21]
	v_lshlrev_b32_e32 v16, 16, v240
	v_and_b32_e32 v17, 0xffff0000, v240
	v_lshlrev_b32_e32 v18, 16, v241
	v_and_b32_e32 v19, 0xffff0000, v241
	v_lshlrev_b32_e32 v20, 16, v242
	v_and_b32_e32 v21, 0xffff0000, v242
	v_lshlrev_b32_e32 v22, 16, v243
	v_and_b32_e32 v23, 0xffff0000, v243
	v_pk_add_f32 v[14:15], v[14:15], v[18:19]
	v_pk_add_f32 v[12:13], v[12:13], v[16:17]
	v_pk_add_f32 v[16:17], v[10:11], v[22:23]
	v_pk_add_f32 v[10:11], v[8:9], v[20:21]
	v_mul_f32_e32 v8, v13, v13
	v_mul_f32_e32 v9, v15, v15
	v_fmac_f32_e32 v8, v12, v12
	v_fmac_f32_e32 v9, v14, v14
	v_add_f32_e32 v8, v8, v9
	v_mul_f32_e32 v9, v11, v11
	v_mul_f32_e32 v18, v17, v17
	v_fmac_f32_e32 v9, v10, v10
	v_fmac_f32_e32 v18, v16, v16
	v_readlane_b32 s2, v252, 8
	v_add_f32_e32 v9, v9, v18
	v_readlane_b32 s3, v252, 9
	v_add_f32_e32 v18, v8, v9
	v_cvt_pk_bf16_f32 v8, v12, v13
	v_cvt_pk_bf16_f32 v9, v14, v15
	v_cvt_pk_bf16_f32 v10, v10, v11
	v_cvt_pk_bf16_f32 v11, v16, v17
	s_nop 0
	v_lshl_add_u64 v[12:13], s[2:3], 0, v[88:89]
	v_lshl_add_u64 v[12:13], v[164:165], 1, v[12:13]
	global_store_dwordx4 v[12:13], v[8:11], off sc1
	s_nop 1
	v_lshlrev_b32_e32 v8, 16, v244
	v_and_b32_e32 v9, 0xffff0000, v244
	v_lshlrev_b32_e32 v10, 16, v245
	v_and_b32_e32 v11, 0xffff0000, v245
	v_lshlrev_b32_e32 v14, 16, v246
	v_and_b32_e32 v15, 0xffff0000, v246
	v_lshlrev_b32_e32 v16, 16, v247
	v_and_b32_e32 v17, 0xffff0000, v247
	v_pk_add_f32 v[6:7], v[6:7], v[10:11]
	v_pk_add_f32 v[4:5], v[4:5], v[8:9]
	v_pk_add_f32 v[8:9], v[2:3], v[16:17]
	v_pk_add_f32 v[2:3], v[0:1], v[14:15]
	v_mul_f32_e32 v0, v5, v5
	v_mul_f32_e32 v1, v7, v7
	v_fmac_f32_e32 v0, v4, v4
	v_fmac_f32_e32 v1, v6, v6
	v_add_f32_e32 v0, v0, v1
	v_mul_f32_e32 v1, v3, v3
	v_mul_f32_e32 v10, v9, v9
	v_fmac_f32_e32 v1, v2, v2
	v_fmac_f32_e32 v10, v8, v8
	v_add_f32_e32 v1, v1, v10
	v_add_f32_e32 v0, v0, v1
	v_add_f32_e32 v10, v18, v0
	v_cvt_pk_bf16_f32 v0, v4, v5
	v_cvt_pk_bf16_f32 v1, v6, v7
	ds_swizzle_b32 v6, v10 offset:swizzle(SWAP,16)
	s_mov_b64 s[2:3], 0x100
	v_cvt_pk_bf16_f32 v2, v2, v3
	v_cvt_pk_bf16_f32 v3, v8, v9
	v_lshl_add_u64 v[4:5], v[12:13], 0, s[2:3]
	global_store_dwordx4 v[4:5], v[0:3], off sc1
	s_nop 1
	s_waitcnt lgkmcnt(0)
	v_add_f32_e32 v0, v10, v6
	v_mov_b32_e32 v1, v0
	s_nop 1
	v_permlane32_swap_b32_e32 v0, v1
	s_and_saveexec_b64 s[20:21], s[0:1]
	v_add_f32_e32 v0, v0, v1
	ds_write_b32 v186, v0 offset:2816
	s_or_b64 exec, exec, s[20:21]
	s_waitcnt lgkmcnt(0)
	s_barrier
	s_and_saveexec_b64 s[20:21], s[10:11]
	s_cbranch_execz .LBB0_1237
	v_add_u32_e32 v0, s5, v182
	v_ashrrev_i32_e32 v1, 31, v0
	v_readlane_b32 s2, v251, 32
	v_lshlrev_b64 v[0:1], 6, v[0:1]
	v_readlane_b32 s3, v251, 33
	s_nop 1
	v_lshl_add_u64 v[0:1], s[2:3], 0, v[0:1]
	s_lshl_b32 s2, s41, 2
	s_ashr_i32 s3, s2, 31
	v_lshl_add_u64 v[4:5], s[2:3], 2, v[0:1]
	ds_read_b128 v[0:3], v185
	s_waitcnt lgkmcnt(0)
	global_store_dwordx4 v[4:5], v[0:3], off sc1
	s_nop 1
